# router phases: row load loop de-serialized (all 24 loads of a row in flight, counted vmcnt), nt on D/OUT2 loads in P10
# speedup vs baseline: 1.0306x; 1.0220x over previous
; DI float bflo(unsigned w) { return __uint_as_float(w << 16); }
; DI float bfhi(unsigned w) { return __uint_as_float(w & 0xffff0000u); }
; DI void phase_router(const Params& p, LAS unsigned char* lds, int G, int bid, const int layer, const float* xin_ctx, const float* xin_lat, const int row_lo, const int row_hi) {
;     ...
;         for (int rr = 0; rr < 2; ++rr) {
;             const int lr = 2 * wave + rr, row = row_lo + bt * 16 + lr;
;             const float* xr = row < NCTX ? xin_ctx + (size_t)row * DM : xin_lat + (size_t)(row - NCTX) * DM;
;             const bf16_t* dr = (const bf16_t*)(p.ws + WS_D) + (size_t)row * DM;
;             const float* md = MOD + (size_t)row_mod(row) * MODN;
;             f32x4 v[8]; float ss = 0.f;
; #pragma unroll
;             for (int i = 0; i < 8; ++i) {
;                 const int col = 4 * lane + 256 * i;
;                 const u32x2 dw = *(const u32x2*)(dr + col);
;                 v[i] = *(const f32x4*)(xr + col) + *(const f32x4*)(md + 2 * DM + col) * (f32x4){bflo(dw.x), bfhi(dw.x), bflo(dw.y), bfhi(dw.y)};
;                 ss += v[i][0] * v[i][0] + v[i][1] * v[i][1] + v[i][2] * v[i][2] + v[i][3] * v[i][3];
;             }
.Lrt7_rows:
	v_readlane_b32 s100, v251, 20
	v_readlane_b32 s101, v251, 21
	v_readfirstlane_b32 s55, v0
	v_and_b32_e32 v33, 63, v0
	v_lshlrev_b32_e32 v27, 4, v33
	v_lshlrev_b32_e32 v31, 3, v33
	v_lshlrev_b32_e32 v33, 2, v33
	v_add_u32_e32 v29, 0x1000, v27
	s_lshr_b32 s55, s55, 6
	s_mov_b32 s13, 0xc3e00000
	s_lshl_b32 s59, s55, 1
	s_add_i32 s58, s54, s59
	s_mul_i32 s59, s59, 0x2010
	v_add_u32_e32 v35, s59, v27
	s_sub_i32 s12, s58, 0x400
	s_cmp_lt_u32 s58, 0x400
	s_cselect_b32 s12, s58, s12
	s_cselect_b32 s74, s56, s52
	s_cselect_b32 s75, s57, s53
	s_lshl_b32 s12, s12, 13
	s_add_u32 s74, s74, s12
	s_addc_u32 s75, s75, 0
	s_lshl_b32 s12, s58, 12
	s_add_u32 s76, s50, s12
	s_addc_u32 s77, s51, 0
	s_add_u32 s76, s76, 0x3af76000
	s_addc_u32 s77, s77, 0
	s_lshl_b32 s12, s58, 11
	s_add_u32 s78, s50, s12
	s_addc_u32 s79, s51, 0
	s_add_u32 s78, s78, 0x41b76000
	s_addc_u32 s79, s79, 0
	s_sub_i32 s12, s58, 0x400
	s_lshr_b32 s12, s12, 11
	s_cmp_lt_u32 s58, 0x400
	s_cselect_b32 s12, 4, s12
	s_mul_i32 s12, s12, 0xc000
	s_add_u32 s80, s50, s12
	s_addc_u32 s81, s51, 0
	s_add_u32 s80, s80, 0x14000
	s_addc_u32 s81, s81, 0
	s_add_u32 s82, s80, 0x2000
	s_addc_u32 s83, s81, 0
	s_add_u32 s98, s80, 0x4000
	s_addc_u32 s99, s81, 0
	global_load_dwordx2 v[2:3], v31, s[76:77] offset:0 nt
	global_load_dwordx4 v[40:43], v27, s[74:75] offset:0 nt
	global_load_dwordx4 v[228:231], v27, s[80:81] offset:0
	global_load_dwordx2 v[4:5], v31, s[76:77] offset:512 nt
	global_load_dwordx4 v[44:47], v27, s[74:75] offset:1024 nt
	global_load_dwordx4 v[232:235], v27, s[80:81] offset:1024
	global_load_dwordx2 v[6:7], v31, s[76:77] offset:1024 nt
	global_load_dwordx4 v[48:51], v27, s[74:75] offset:2048 nt
	global_load_dwordx4 v[236:239], v27, s[80:81] offset:2048
	global_load_dwordx2 v[8:9], v31, s[76:77] offset:1536 nt
	global_load_dwordx4 v[52:55], v27, s[74:75] offset:3072 nt
	global_load_dwordx4 v[240:243], v27, s[80:81] offset:3072
	global_load_dwordx2 v[216:217], v31, s[76:77] offset:2048 nt
	global_load_dwordx4 v[56:59], v29, s[74:75] offset:0 nt
	global_load_dwordx4 v[244:247], v29, s[80:81] offset:0
	global_load_dwordx2 v[218:219], v31, s[76:77] offset:2560 nt
	global_load_dwordx4 v[60:63], v29, s[74:75] offset:1024 nt
	global_load_dwordx2 v[220:221], v31, s[76:77] offset:3072 nt
	global_load_dwordx4 v[64:67], v29, s[74:75] offset:2048 nt
	global_load_dwordx2 v[224:225], v31, s[76:77] offset:3584 nt
	global_load_dwordx4 v[68:71], v29, s[74:75] offset:3072 nt
	s_waitcnt vmcnt(18)
	v_and_b32_e32 v223, 0xffff0000, v2
	v_and_b32_e32 v250, 0xffff0000, v3
	v_lshlrev_b32_e32 v2, 16, v2
	v_lshlrev_b32_e32 v3, 16, v3
	v_fmac_f32_e32 v40, v228, v2
	v_fmac_f32_e32 v41, v229, v223
	v_fmac_f32_e32 v42, v230, v3
	v_fmac_f32_e32 v43, v231, v250
	global_load_dwordx4 v[228:231], v29, s[80:81] offset:1024
	v_mul_f32_e32 v226, v41, v41
	v_fmac_f32_e32 v226, v40, v40
	v_fmac_f32_e32 v226, v42, v42
	v_fmac_f32_e32 v226, v43, v43
	s_waitcnt vmcnt(16)
	v_and_b32_e32 v223, 0xffff0000, v4
	v_and_b32_e32 v250, 0xffff0000, v5
	v_lshlrev_b32_e32 v4, 16, v4
	v_lshlrev_b32_e32 v5, 16, v5
	v_fmac_f32_e32 v44, v232, v4
	v_fmac_f32_e32 v45, v233, v223
	v_fmac_f32_e32 v46, v234, v5
	v_fmac_f32_e32 v47, v235, v250
	global_load_dwordx4 v[232:235], v29, s[80:81] offset:2048
	v_mul_f32_e32 v223, v45, v45
	v_fmac_f32_e32 v223, v44, v44
	v_fmac_f32_e32 v223, v46, v46
	v_fmac_f32_e32 v223, v47, v47
	v_add_f32_e32 v226, v226, v223
	s_waitcnt vmcnt(14)
	v_and_b32_e32 v223, 0xffff0000, v6
	v_and_b32_e32 v250, 0xffff0000, v7
	v_lshlrev_b32_e32 v6, 16, v6
	v_lshlrev_b32_e32 v7, 16, v7
	v_fmac_f32_e32 v48, v236, v6
	v_fmac_f32_e32 v49, v237, v223
	v_fmac_f32_e32 v50, v238, v7
	v_fmac_f32_e32 v51, v239, v250
	global_load_dwordx4 v[236:239], v29, s[80:81] offset:3072
	v_mul_f32_e32 v223, v49, v49
	v_fmac_f32_e32 v223, v48, v48
	v_fmac_f32_e32 v223, v50, v50
	v_fmac_f32_e32 v223, v51, v51
	v_add_f32_e32 v226, v226, v223
	s_waitcnt vmcnt(12)
	v_and_b32_e32 v223, 0xffff0000, v8
	v_and_b32_e32 v250, 0xffff0000, v9
	v_lshlrev_b32_e32 v8, 16, v8
	v_lshlrev_b32_e32 v9, 16, v9
	v_fmac_f32_e32 v52, v240, v8
	v_fmac_f32_e32 v53, v241, v223
	v_fmac_f32_e32 v54, v242, v9
	v_fmac_f32_e32 v55, v243, v250
	v_mul_f32_e32 v223, v53, v53
	v_fmac_f32_e32 v223, v52, v52
	v_fmac_f32_e32 v223, v54, v54
	v_fmac_f32_e32 v223, v55, v55
	v_add_f32_e32 v226, v226, v223
	s_waitcnt vmcnt(9)
	v_and_b32_e32 v223, 0xffff0000, v216
	v_and_b32_e32 v250, 0xffff0000, v217
	v_lshlrev_b32_e32 v216, 16, v216
	v_lshlrev_b32_e32 v217, 16, v217
	v_fmac_f32_e32 v56, v244, v216
	v_fmac_f32_e32 v57, v245, v223
	v_fmac_f32_e32 v58, v246, v217
	v_fmac_f32_e32 v59, v247, v250
	v_mul_f32_e32 v223, v57, v57
	v_fmac_f32_e32 v223, v56, v56
	v_fmac_f32_e32 v223, v58, v58
	v_fmac_f32_e32 v223, v59, v59
	v_add_f32_e32 v226, v226, v223
	s_waitcnt vmcnt(2)
	v_and_b32_e32 v223, 0xffff0000, v218
	v_and_b32_e32 v250, 0xffff0000, v219
	v_lshlrev_b32_e32 v218, 16, v218
	v_lshlrev_b32_e32 v219, 16, v219
	v_fmac_f32_e32 v60, v228, v218
	v_fmac_f32_e32 v61, v229, v223
	v_fmac_f32_e32 v62, v230, v219
	v_fmac_f32_e32 v63, v231, v250
	v_mul_f32_e32 v223, v61, v61
	v_fmac_f32_e32 v223, v60, v60
	v_fmac_f32_e32 v223, v62, v62
	v_fmac_f32_e32 v223, v63, v63
	v_add_f32_e32 v226, v226, v223
	s_waitcnt vmcnt(1)
	v_and_b32_e32 v223, 0xffff0000, v220
	v_and_b32_e32 v250, 0xffff0000, v221
	v_lshlrev_b32_e32 v220, 16, v220
	v_lshlrev_b32_e32 v221, 16, v221
	v_fmac_f32_e32 v64, v232, v220
	v_fmac_f32_e32 v65, v233, v223
	v_fmac_f32_e32 v66, v234, v221
	v_fmac_f32_e32 v67, v235, v250
	v_mul_f32_e32 v223, v65, v65
	v_fmac_f32_e32 v223, v64, v64
	v_fmac_f32_e32 v223, v66, v66
	v_fmac_f32_e32 v223, v67, v67
	v_add_f32_e32 v226, v226, v223
	s_waitcnt vmcnt(0)
; #define LAS __attribute__((address_space(3)))
; DI unsigned pk_bf16(float lo, float hi) { f32x2 v = {lo, hi}; hbf16x2 r = __builtin_convertvector(v, hbf16x2); return __builtin_bit_cast(unsigned, r); }
; DI void phase_router(const Params& p, LAS unsigned char* lds, int G, int bid, const int layer, const float* xin_ctx, const float* xin_lat, const int row_lo, const int row_hi) {
;     ...
;             }
;             ss = wave_sum(ss);
;             const float r = rsqrtf(ss * (1.0f / DM) + EPS);
; #pragma unroll
;             for (int i = 0; i < 8; ++i) {
;                 const int col = 4 * lane + 256 * i;
;                 const f32x4 g = *(const f32x4*)(gain + col), sh = *(const f32x4*)(md + 3 * DM + col), scl = *(const f32x4*)(md + 4 * DM + col);
;                 const f32x4 hv = (v[i] * r * g) * (1.0f + scl) + sh;
;                 if (layer == 0 && !FP8_L0) { u32x2 w; w.x = pk_bf16(hv[0], hv[1]); w.y = pk_bf16(hv[2], hv[3]); *(u32x2*)(H + (size_t)row * DM + col) = w; }
;                 else *(unsigned*)(p.ws + WS_H8 + (size_t)row * DM + col) = pk_fp8x4(hv[0], hv[1], hv[2], hv[3]);
;                 *(LAS f32x4*)(hs + lr * RT_HS + col) = hv;
;             }
	v_and_b32_e32 v223, 0xffff0000, v224
	v_and_b32_e32 v250, 0xffff0000, v225
	v_lshlrev_b32_e32 v224, 16, v224
	v_lshlrev_b32_e32 v225, 16, v225
	v_fmac_f32_e32 v68, v236, v224
	v_fmac_f32_e32 v69, v237, v223
	v_fmac_f32_e32 v70, v238, v225
	v_fmac_f32_e32 v71, v239, v250
	v_mul_f32_e32 v223, v69, v69
	v_fmac_f32_e32 v223, v68, v68
	v_fmac_f32_e32 v223, v70, v70
	v_fmac_f32_e32 v223, v71, v71
	v_add_f32_e32 v226, v226, v223
	global_load_dwordx4 v[228:231], v27, s[100:101] offset:0
	global_load_dwordx4 v[232:235], v27, s[82:83] offset:0
	global_load_dwordx4 v[236:239], v27, s[98:99] offset:0
	global_load_dwordx4 v[240:243], v27, s[100:101] offset:1024
	global_load_dwordx4 v[244:247], v27, s[82:83] offset:1024
	global_load_dwordx4 v[216:219], v27, s[98:99] offset:1024
	global_load_dwordx4 v[2:5], v27, s[100:101] offset:2048
	global_load_dwordx4 v[6:9], v27, s[82:83] offset:2048
	global_load_dwordx2 v[248:249], v27, s[98:99] offset:2048
	global_load_dwordx2 v[220:221], v27, s[98:99] offset:2056
	ds_bpermute_b32 v223, v203, v226
	s_waitcnt lgkmcnt(0)
	v_add_f32_e32 v226, v226, v223
	ds_bpermute_b32 v223, v204, v226
	s_waitcnt lgkmcnt(0)
	v_add_f32_e32 v226, v226, v223
	ds_bpermute_b32 v223, v205, v226
	s_waitcnt lgkmcnt(0)
	v_add_f32_e32 v226, v226, v223
	ds_bpermute_b32 v223, v206, v226
	s_waitcnt lgkmcnt(0)
	v_add_f32_e32 v226, v226, v223
	ds_bpermute_b32 v223, v207, v226
	s_waitcnt lgkmcnt(0)
	v_add_f32_e32 v226, v226, v223
	ds_bpermute_b32 v223, v208, v226
	s_waitcnt lgkmcnt(0)
	v_add_f32_e32 v226, v226, v223
	v_mov_b32_e32 v250, 0x358637bd
	v_fmamk_f32 v226, v226, 0x3a000000, v250
	v_cmp_gt_f32_e32 vcc, 0x800000, v226
	v_mul_f32_e32 v223, 0x4b800000, v226
	s_nop 1
	v_cndmask_b32_e32 v226, v226, v223, vcc
	v_rsq_f32_e32 v226, v226
	s_nop 0
	v_mul_f32_e32 v223, 0x45800000, v226
	v_mov_b32_e32 v250, 0x43e00000
	v_cndmask_b32_e32 v226, v226, v223, vcc
	s_waitcnt vmcnt(7)
	v_pk_mul_f32 v[40:41], v[40:41], v[226:227] op_sel_hi:[1,0]
	v_pk_mul_f32 v[42:43], v[42:43], v[226:227] op_sel_hi:[1,0]
	v_pk_add_f32 v[236:237], v[236:237], 1.0 op_sel_hi:[1,0]
	v_pk_add_f32 v[238:239], v[238:239], 1.0 op_sel_hi:[1,0]
	v_pk_mul_f32 v[40:41], v[228:229], v[40:41]
	v_pk_mul_f32 v[42:43], v[230:231], v[42:43]
	v_pk_fma_f32 v[40:41], v[236:237], v[40:41], v[232:233]
	v_pk_fma_f32 v[42:43], v[238:239], v[42:43], v[234:235]
	v_med3_f32 v228, v40, s13, v250
	v_med3_f32 v229, v41, s13, v250
	v_med3_f32 v230, v42, s13, v250
	v_med3_f32 v231, v43, s13, v250
	ds_write_b128 v35, v[40:43] offset:0
	v_cvt_pk_fp8_f32 v224, v228, v229
	v_cvt_pk_fp8_f32 v224, v230, v231 op_sel:[0,0,1]
	s_nop 0
	global_store_dword v33, v224, s[78:79] offset:0
	global_load_dwordx4 v[228:231], v27, s[100:101] offset:3072
	global_load_dwordx4 v[232:235], v27, s[82:83] offset:3072
	global_load_dwordx4 v[236:239], v27, s[98:99] offset:3072
	s_waitcnt vmcnt(8)
	v_pk_mul_f32 v[44:45], v[44:45], v[226:227] op_sel_hi:[1,0]
	v_pk_mul_f32 v[46:47], v[46:47], v[226:227] op_sel_hi:[1,0]
	v_pk_add_f32 v[216:217], v[216:217], 1.0 op_sel_hi:[1,0]
	v_pk_add_f32 v[218:219], v[218:219], 1.0 op_sel_hi:[1,0]
	v_pk_mul_f32 v[44:45], v[240:241], v[44:45]
	v_pk_mul_f32 v[46:47], v[242:243], v[46:47]
	v_pk_fma_f32 v[44:45], v[216:217], v[44:45], v[244:245]
	v_pk_fma_f32 v[46:47], v[218:219], v[46:47], v[246:247]
	v_med3_f32 v240, v44, s13, v250
	v_med3_f32 v241, v45, s13, v250
	v_med3_f32 v242, v46, s13, v250
	v_med3_f32 v243, v47, s13, v250
	ds_write_b128 v35, v[44:47] offset:1024
	v_cvt_pk_fp8_f32 v225, v240, v241
	v_cvt_pk_fp8_f32 v225, v242, v243 op_sel:[0,0,1]
	s_nop 0
	global_store_dword v33, v225, s[78:79] offset:256
	global_load_dwordx4 v[240:243], v29, s[100:101] offset:0
	global_load_dwordx4 v[244:247], v29, s[82:83] offset:0
	global_load_dwordx4 v[216:219], v29, s[98:99] offset:0
	s_waitcnt vmcnt(8)
	v_pk_mul_f32 v[48:49], v[48:49], v[226:227] op_sel_hi:[1,0]
	v_pk_mul_f32 v[50:51], v[50:51], v[226:227] op_sel_hi:[1,0]
	v_pk_add_f32 v[248:249], v[248:249], 1.0 op_sel_hi:[1,0]
	v_pk_add_f32 v[220:221], v[220:221], 1.0 op_sel_hi:[1,0]
	v_pk_mul_f32 v[48:49], v[2:3], v[48:49]
	v_pk_mul_f32 v[50:51], v[4:5], v[50:51]
	v_pk_fma_f32 v[48:49], v[248:249], v[48:49], v[6:7]
	v_pk_fma_f32 v[50:51], v[220:221], v[50:51], v[8:9]
	v_med3_f32 v2, v48, s13, v250
	v_med3_f32 v3, v49, s13, v250
	v_med3_f32 v4, v50, s13, v250
	v_med3_f32 v5, v51, s13, v250
	ds_write_b128 v35, v[48:51] offset:2048
	v_cvt_pk_fp8_f32 v215, v2, v3
	v_cvt_pk_fp8_f32 v215, v4, v5 op_sel:[0,0,1]
	s_nop 0
	global_store_dword v33, v215, s[78:79] offset:512
	global_load_dwordx4 v[2:5], v29, s[100:101] offset:1024
	global_load_dwordx4 v[6:9], v29, s[82:83] offset:1024
	global_load_dwordx2 v[248:249], v29, s[98:99] offset:1024
	global_load_dwordx2 v[220:221], v29, s[98:99] offset:1032
	s_waitcnt vmcnt(9)
	v_pk_mul_f32 v[52:53], v[52:53], v[226:227] op_sel_hi:[1,0]
	v_pk_mul_f32 v[54:55], v[54:55], v[226:227] op_sel_hi:[1,0]
	v_pk_add_f32 v[236:237], v[236:237], 1.0 op_sel_hi:[1,0]
	v_pk_add_f32 v[238:239], v[238:239], 1.0 op_sel_hi:[1,0]
	v_pk_mul_f32 v[52:53], v[228:229], v[52:53]
	v_pk_mul_f32 v[54:55], v[230:231], v[54:55]
	v_pk_fma_f32 v[52:53], v[236:237], v[52:53], v[232:233]
	v_pk_fma_f32 v[54:55], v[238:239], v[54:55], v[234:235]
	v_med3_f32 v228, v52, s13, v250
	v_med3_f32 v229, v53, s13, v250
	v_med3_f32 v230, v54, s13, v250
	v_med3_f32 v231, v55, s13, v250
	ds_write_b128 v35, v[52:55] offset:3072
	v_cvt_pk_fp8_f32 v224, v228, v229
	v_cvt_pk_fp8_f32 v224, v230, v231 op_sel:[0,0,1]
	s_nop 0
	global_store_dword v33, v224, s[78:79] offset:768
	global_load_dwordx4 v[228:231], v29, s[100:101] offset:2048
	global_load_dwordx4 v[232:235], v29, s[82:83] offset:2048
	global_load_dwordx4 v[236:239], v29, s[98:99] offset:2048
	s_waitcnt vmcnt(9)
; #define LAS __attribute__((address_space(3)))
; DI unsigned pk_bf16(float lo, float hi) { f32x2 v = {lo, hi}; hbf16x2 r = __builtin_convertvector(v, hbf16x2); return __builtin_bit_cast(unsigned, r); }
; DI float bflo(unsigned w) { return __uint_as_float(w << 16); }
; DI float bfhi(unsigned w) { return __uint_as_float(w & 0xffff0000u); }
; DI void phase_router(const Params& p, LAS unsigned char* lds, int G, int bid, const int layer, const float* xin_ctx, const float* xin_lat, const int row_lo, const int row_hi) {
;     ...
;             const int lr = 2 * wave + rr, row = row_lo + bt * 16 + lr;
;             const float* xr = row < NCTX ? xin_ctx + (size_t)row * DM : xin_lat + (size_t)(row - NCTX) * DM;
;             const bf16_t* dr = (const bf16_t*)(p.ws + WS_D) + (size_t)row * DM;
;             const float* md = MOD + (size_t)row_mod(row) * MODN;
;             f32x4 v[8]; float ss = 0.f;
; #pragma unroll
;             for (int i = 0; i < 8; ++i) {
;                 const int col = 4 * lane + 256 * i;
;                 const u32x2 dw = *(const u32x2*)(dr + col);
;                 v[i] = *(const f32x4*)(xr + col) + *(const f32x4*)(md + 2 * DM + col) * (f32x4){bflo(dw.x), bfhi(dw.x), bflo(dw.y), bfhi(dw.y)};
;                 ss += v[i][0] * v[i][0] + v[i][1] * v[i][1] + v[i][2] * v[i][2] + v[i][3] * v[i][3];
;     ...
; #pragma unroll
;             for (int i = 0; i < 8; ++i) {
;                 const int col = 4 * lane + 256 * i;
;                 const f32x4 g = *(const f32x4*)(gain + col), sh = *(const f32x4*)(md + 3 * DM + col), scl = *(const f32x4*)(md + 4 * DM + col);
;                 const f32x4 hv = (v[i] * r * g) * (1.0f + scl) + sh;
;                 if (layer == 0 && !FP8_L0) { u32x2 w; w.x = pk_bf16(hv[0], hv[1]); w.y = pk_bf16(hv[2], hv[3]); *(u32x2*)(H + (size_t)row * DM + col) = w; }
;                 else *(unsigned*)(p.ws + WS_H8 + (size_t)row * DM + col) = pk_fp8x4(hv[0], hv[1], hv[2], hv[3]);
;                 *(LAS f32x4*)(hs + lr * RT_HS + col) = hv;
;             }
	v_pk_mul_f32 v[56:57], v[56:57], v[226:227] op_sel_hi:[1,0]
	v_pk_mul_f32 v[58:59], v[58:59], v[226:227] op_sel_hi:[1,0]
	v_pk_add_f32 v[216:217], v[216:217], 1.0 op_sel_hi:[1,0]
	v_pk_add_f32 v[218:219], v[218:219], 1.0 op_sel_hi:[1,0]
	v_pk_mul_f32 v[56:57], v[240:241], v[56:57]
	v_pk_mul_f32 v[58:59], v[242:243], v[58:59]
	v_pk_fma_f32 v[56:57], v[216:217], v[56:57], v[244:245]
	v_pk_fma_f32 v[58:59], v[218:219], v[58:59], v[246:247]
	v_med3_f32 v240, v56, s13, v250
	v_med3_f32 v241, v57, s13, v250
	v_med3_f32 v242, v58, s13, v250
	v_med3_f32 v243, v59, s13, v250
	ds_write_b128 v35, v[56:59] offset:4096
	v_cvt_pk_fp8_f32 v225, v240, v241
	v_cvt_pk_fp8_f32 v225, v242, v243 op_sel:[0,0,1]
	s_nop 0
	global_store_dword v33, v225, s[78:79] offset:1024
	global_load_dwordx4 v[240:243], v29, s[100:101] offset:3072
	global_load_dwordx4 v[244:247], v29, s[82:83] offset:3072
	global_load_dwordx4 v[216:219], v29, s[98:99] offset:3072
	s_waitcnt vmcnt(8)
	v_pk_mul_f32 v[60:61], v[60:61], v[226:227] op_sel_hi:[1,0]
	v_pk_mul_f32 v[62:63], v[62:63], v[226:227] op_sel_hi:[1,0]
	v_pk_add_f32 v[248:249], v[248:249], 1.0 op_sel_hi:[1,0]
	v_pk_add_f32 v[220:221], v[220:221], 1.0 op_sel_hi:[1,0]
	v_pk_mul_f32 v[60:61], v[2:3], v[60:61]
	v_pk_mul_f32 v[62:63], v[4:5], v[62:63]
	v_pk_fma_f32 v[60:61], v[248:249], v[60:61], v[6:7]
	v_pk_fma_f32 v[62:63], v[220:221], v[62:63], v[8:9]
	v_med3_f32 v2, v60, s13, v250
	v_med3_f32 v3, v61, s13, v250
	v_med3_f32 v4, v62, s13, v250
	v_med3_f32 v5, v63, s13, v250
	ds_write_b128 v35, v[60:63] offset:5120
	v_cvt_pk_fp8_f32 v215, v2, v3
	v_cvt_pk_fp8_f32 v215, v4, v5 op_sel:[0,0,1]
	s_nop 0
	global_store_dword v33, v215, s[78:79] offset:1280
	s_waitcnt vmcnt(5)
	v_pk_mul_f32 v[64:65], v[64:65], v[226:227] op_sel_hi:[1,0]
	v_pk_mul_f32 v[66:67], v[66:67], v[226:227] op_sel_hi:[1,0]
	v_pk_add_f32 v[236:237], v[236:237], 1.0 op_sel_hi:[1,0]
	v_pk_add_f32 v[238:239], v[238:239], 1.0 op_sel_hi:[1,0]
	v_pk_mul_f32 v[64:65], v[228:229], v[64:65]
	v_pk_mul_f32 v[66:67], v[230:231], v[66:67]
	v_pk_fma_f32 v[64:65], v[236:237], v[64:65], v[232:233]
	v_pk_fma_f32 v[66:67], v[238:239], v[66:67], v[234:235]
	v_med3_f32 v228, v64, s13, v250
	v_med3_f32 v229, v65, s13, v250
	v_med3_f32 v230, v66, s13, v250
	v_med3_f32 v231, v67, s13, v250
	ds_write_b128 v35, v[64:67] offset:6144
	v_cvt_pk_fp8_f32 v224, v228, v229
	v_cvt_pk_fp8_f32 v224, v230, v231 op_sel:[0,0,1]
	s_nop 0
	global_store_dword v33, v224, s[78:79] offset:1536
	s_waitcnt vmcnt(2)
	v_pk_mul_f32 v[68:69], v[68:69], v[226:227] op_sel_hi:[1,0]
	v_pk_mul_f32 v[70:71], v[70:71], v[226:227] op_sel_hi:[1,0]
	v_pk_add_f32 v[216:217], v[216:217], 1.0 op_sel_hi:[1,0]
	v_pk_add_f32 v[218:219], v[218:219], 1.0 op_sel_hi:[1,0]
	v_pk_mul_f32 v[68:69], v[240:241], v[68:69]
	v_pk_mul_f32 v[70:71], v[242:243], v[70:71]
	v_pk_fma_f32 v[68:69], v[216:217], v[68:69], v[244:245]
	v_pk_fma_f32 v[70:71], v[218:219], v[70:71], v[246:247]
	v_med3_f32 v240, v68, s13, v250
	v_med3_f32 v241, v69, s13, v250
	v_med3_f32 v242, v70, s13, v250
	v_med3_f32 v243, v71, s13, v250
	ds_write_b128 v35, v[68:71] offset:7168
	v_cvt_pk_fp8_f32 v225, v240, v241
	v_cvt_pk_fp8_f32 v225, v242, v243 op_sel:[0,0,1]
	s_nop 0
	global_store_dword v33, v225, s[78:79] offset:1792
	s_lshl_b32 s59, s55, 1
	s_add_i32 s59, s59, 1
	s_add_i32 s58, s54, s59
	s_mul_i32 s59, s59, 0x2010
	v_add_u32_e32 v35, s59, v27
	s_sub_i32 s12, s58, 0x400
	s_cmp_lt_u32 s58, 0x400
	s_cselect_b32 s12, s58, s12
	s_cselect_b32 s74, s56, s52
	s_cselect_b32 s75, s57, s53
	s_lshl_b32 s12, s12, 13
	s_add_u32 s74, s74, s12
	s_addc_u32 s75, s75, 0
	s_lshl_b32 s12, s58, 12
	s_add_u32 s76, s50, s12
	s_addc_u32 s77, s51, 0
	s_add_u32 s76, s76, 0x3af76000
	s_addc_u32 s77, s77, 0
	s_lshl_b32 s12, s58, 11
	s_add_u32 s78, s50, s12
	s_addc_u32 s79, s51, 0
	s_add_u32 s78, s78, 0x41b76000
	s_addc_u32 s79, s79, 0
	s_sub_i32 s12, s58, 0x400
	s_lshr_b32 s12, s12, 11
	s_cmp_lt_u32 s58, 0x400
	s_cselect_b32 s12, 4, s12
	s_mul_i32 s12, s12, 0xc000
	s_add_u32 s80, s50, s12
	s_addc_u32 s81, s51, 0
	s_add_u32 s80, s80, 0x14000
	s_addc_u32 s81, s81, 0
	s_add_u32 s82, s80, 0x2000
	s_addc_u32 s83, s81, 0
	s_add_u32 s98, s80, 0x4000
	s_addc_u32 s99, s81, 0
	global_load_dwordx2 v[2:3], v31, s[76:77] offset:0 nt
	global_load_dwordx4 v[40:43], v27, s[74:75] offset:0 nt
	global_load_dwordx4 v[228:231], v27, s[80:81] offset:0
	global_load_dwordx2 v[4:5], v31, s[76:77] offset:512 nt
	global_load_dwordx4 v[44:47], v27, s[74:75] offset:1024 nt
	global_load_dwordx4 v[232:235], v27, s[80:81] offset:1024
	global_load_dwordx2 v[6:7], v31, s[76:77] offset:1024 nt
	global_load_dwordx4 v[48:51], v27, s[74:75] offset:2048 nt
	global_load_dwordx4 v[236:239], v27, s[80:81] offset:2048
	global_load_dwordx2 v[8:9], v31, s[76:77] offset:1536 nt
	global_load_dwordx4 v[52:55], v27, s[74:75] offset:3072 nt
	global_load_dwordx4 v[240:243], v27, s[80:81] offset:3072
	global_load_dwordx2 v[216:217], v31, s[76:77] offset:2048 nt
	global_load_dwordx4 v[56:59], v29, s[74:75] offset:0 nt
	global_load_dwordx4 v[244:247], v29, s[80:81] offset:0
	global_load_dwordx2 v[218:219], v31, s[76:77] offset:2560 nt
	global_load_dwordx4 v[60:63], v29, s[74:75] offset:1024 nt
	global_load_dwordx2 v[220:221], v31, s[76:77] offset:3072 nt
	global_load_dwordx4 v[64:67], v29, s[74:75] offset:2048 nt
	global_load_dwordx2 v[224:225], v31, s[76:77] offset:3584 nt
	global_load_dwordx4 v[68:71], v29, s[74:75] offset:3072 nt
	s_waitcnt vmcnt(18)
; #define LAS __attribute__((address_space(3)))
; DI unsigned pk_bf16(float lo, float hi) { f32x2 v = {lo, hi}; hbf16x2 r = __builtin_convertvector(v, hbf16x2); return __builtin_bit_cast(unsigned, r); }
; DI float bflo(unsigned w) { return __uint_as_float(w << 16); }
; DI float bfhi(unsigned w) { return __uint_as_float(w & 0xffff0000u); }
; DI void phase_router(const Params& p, LAS unsigned char* lds, int G, int bid, const int layer, const float* xin_ctx, const float* xin_lat, const int row_lo, const int row_hi) {
;     ...
;             for (int i = 0; i < 8; ++i) {
;                 const int col = 4 * lane + 256 * i;
;                 const u32x2 dw = *(const u32x2*)(dr + col);
;                 v[i] = *(const f32x4*)(xr + col) + *(const f32x4*)(md + 2 * DM + col) * (f32x4){bflo(dw.x), bfhi(dw.x), bflo(dw.y), bfhi(dw.y)};
;                 ss += v[i][0] * v[i][0] + v[i][1] * v[i][1] + v[i][2] * v[i][2] + v[i][3] * v[i][3];
;             }
;             ss = wave_sum(ss);
;             const float r = rsqrtf(ss * (1.0f / DM) + EPS);
; #pragma unroll
;             for (int i = 0; i < 8; ++i) {
;                 const int col = 4 * lane + 256 * i;
;                 const f32x4 g = *(const f32x4*)(gain + col), sh = *(const f32x4*)(md + 3 * DM + col), scl = *(const f32x4*)(md + 4 * DM + col);
;                 const f32x4 hv = (v[i] * r * g) * (1.0f + scl) + sh;
;                 if (layer == 0 && !FP8_L0) { u32x2 w; w.x = pk_bf16(hv[0], hv[1]); w.y = pk_bf16(hv[2], hv[3]); *(u32x2*)(H + (size_t)row * DM + col) = w; }
;                 else *(unsigned*)(p.ws + WS_H8 + (size_t)row * DM + col) = pk_fp8x4(hv[0], hv[1], hv[2], hv[3]);
;                 *(LAS f32x4*)(hs + lr * RT_HS + col) = hv;
;             }
	v_and_b32_e32 v223, 0xffff0000, v2
	v_and_b32_e32 v250, 0xffff0000, v3
	v_lshlrev_b32_e32 v2, 16, v2
	v_lshlrev_b32_e32 v3, 16, v3
	v_fmac_f32_e32 v40, v228, v2
	v_fmac_f32_e32 v41, v229, v223
	v_fmac_f32_e32 v42, v230, v3
	v_fmac_f32_e32 v43, v231, v250
	global_load_dwordx4 v[228:231], v29, s[80:81] offset:1024
	v_mul_f32_e32 v226, v41, v41
	v_fmac_f32_e32 v226, v40, v40
	v_fmac_f32_e32 v226, v42, v42
	v_fmac_f32_e32 v226, v43, v43
	s_waitcnt vmcnt(16)
	v_and_b32_e32 v223, 0xffff0000, v4
	v_and_b32_e32 v250, 0xffff0000, v5
	v_lshlrev_b32_e32 v4, 16, v4
	v_lshlrev_b32_e32 v5, 16, v5
	v_fmac_f32_e32 v44, v232, v4
	v_fmac_f32_e32 v45, v233, v223
	v_fmac_f32_e32 v46, v234, v5
	v_fmac_f32_e32 v47, v235, v250
	global_load_dwordx4 v[232:235], v29, s[80:81] offset:2048
	v_mul_f32_e32 v223, v45, v45
	v_fmac_f32_e32 v223, v44, v44
	v_fmac_f32_e32 v223, v46, v46
	v_fmac_f32_e32 v223, v47, v47
	v_add_f32_e32 v226, v226, v223
	s_waitcnt vmcnt(14)
	v_and_b32_e32 v223, 0xffff0000, v6
	v_and_b32_e32 v250, 0xffff0000, v7
	v_lshlrev_b32_e32 v6, 16, v6
	v_lshlrev_b32_e32 v7, 16, v7
	v_fmac_f32_e32 v48, v236, v6
	v_fmac_f32_e32 v49, v237, v223
	v_fmac_f32_e32 v50, v238, v7
	v_fmac_f32_e32 v51, v239, v250
	global_load_dwordx4 v[236:239], v29, s[80:81] offset:3072
	v_mul_f32_e32 v223, v49, v49
	v_fmac_f32_e32 v223, v48, v48
	v_fmac_f32_e32 v223, v50, v50
	v_fmac_f32_e32 v223, v51, v51
	v_add_f32_e32 v226, v226, v223
	s_waitcnt vmcnt(12)
	v_and_b32_e32 v223, 0xffff0000, v8
	v_and_b32_e32 v250, 0xffff0000, v9
	v_lshlrev_b32_e32 v8, 16, v8
	v_lshlrev_b32_e32 v9, 16, v9
	v_fmac_f32_e32 v52, v240, v8
	v_fmac_f32_e32 v53, v241, v223
	v_fmac_f32_e32 v54, v242, v9
	v_fmac_f32_e32 v55, v243, v250
	v_mul_f32_e32 v223, v53, v53
	v_fmac_f32_e32 v223, v52, v52
	v_fmac_f32_e32 v223, v54, v54
	v_fmac_f32_e32 v223, v55, v55
	v_add_f32_e32 v226, v226, v223
	s_waitcnt vmcnt(9)
	v_and_b32_e32 v223, 0xffff0000, v216
	v_and_b32_e32 v250, 0xffff0000, v217
	v_lshlrev_b32_e32 v216, 16, v216
	v_lshlrev_b32_e32 v217, 16, v217
	v_fmac_f32_e32 v56, v244, v216
	v_fmac_f32_e32 v57, v245, v223
	v_fmac_f32_e32 v58, v246, v217
	v_fmac_f32_e32 v59, v247, v250
	v_mul_f32_e32 v223, v57, v57
	v_fmac_f32_e32 v223, v56, v56
	v_fmac_f32_e32 v223, v58, v58
	v_fmac_f32_e32 v223, v59, v59
	v_add_f32_e32 v226, v226, v223
	s_waitcnt vmcnt(2)
	v_and_b32_e32 v223, 0xffff0000, v218
	v_and_b32_e32 v250, 0xffff0000, v219
	v_lshlrev_b32_e32 v218, 16, v218
	v_lshlrev_b32_e32 v219, 16, v219
	v_fmac_f32_e32 v60, v228, v218
	v_fmac_f32_e32 v61, v229, v223
	v_fmac_f32_e32 v62, v230, v219
	v_fmac_f32_e32 v63, v231, v250
	v_mul_f32_e32 v223, v61, v61
	v_fmac_f32_e32 v223, v60, v60
	v_fmac_f32_e32 v223, v62, v62
	v_fmac_f32_e32 v223, v63, v63
	v_add_f32_e32 v226, v226, v223
	s_waitcnt vmcnt(1)
	v_and_b32_e32 v223, 0xffff0000, v220
	v_and_b32_e32 v250, 0xffff0000, v221
	v_lshlrev_b32_e32 v220, 16, v220
	v_lshlrev_b32_e32 v221, 16, v221
	v_fmac_f32_e32 v64, v232, v220
	v_fmac_f32_e32 v65, v233, v223
	v_fmac_f32_e32 v66, v234, v221
	v_fmac_f32_e32 v67, v235, v250
	v_mul_f32_e32 v223, v65, v65
	v_fmac_f32_e32 v223, v64, v64
	v_fmac_f32_e32 v223, v66, v66
	v_fmac_f32_e32 v223, v67, v67
	v_add_f32_e32 v226, v226, v223
	s_waitcnt vmcnt(0)
	v_and_b32_e32 v223, 0xffff0000, v224
	v_and_b32_e32 v250, 0xffff0000, v225
	v_lshlrev_b32_e32 v224, 16, v224
	v_lshlrev_b32_e32 v225, 16, v225
	v_fmac_f32_e32 v68, v236, v224
	v_fmac_f32_e32 v69, v237, v223
	v_fmac_f32_e32 v70, v238, v225
	v_fmac_f32_e32 v71, v239, v250
	v_mul_f32_e32 v223, v69, v69
	v_fmac_f32_e32 v223, v68, v68
	v_fmac_f32_e32 v223, v70, v70
	v_fmac_f32_e32 v223, v71, v71
	v_add_f32_e32 v226, v226, v223
	global_load_dwordx4 v[228:231], v27, s[100:101] offset:0
	global_load_dwordx4 v[232:235], v27, s[82:83] offset:0
	global_load_dwordx4 v[236:239], v27, s[98:99] offset:0
	global_load_dwordx4 v[240:243], v27, s[100:101] offset:1024
	global_load_dwordx4 v[244:247], v27, s[82:83] offset:1024
	global_load_dwordx4 v[216:219], v27, s[98:99] offset:1024
	global_load_dwordx4 v[2:5], v27, s[100:101] offset:2048
	global_load_dwordx4 v[6:9], v27, s[82:83] offset:2048
	global_load_dwordx2 v[248:249], v27, s[98:99] offset:2048
	global_load_dwordx2 v[220:221], v27, s[98:99] offset:2056
	ds_bpermute_b32 v223, v203, v226
	s_waitcnt lgkmcnt(0)
	v_add_f32_e32 v226, v226, v223
	ds_bpermute_b32 v223, v204, v226
	s_waitcnt lgkmcnt(0)
	v_add_f32_e32 v226, v226, v223
	ds_bpermute_b32 v223, v205, v226
	s_waitcnt lgkmcnt(0)
	v_add_f32_e32 v226, v226, v223
	ds_bpermute_b32 v223, v206, v226
	s_waitcnt lgkmcnt(0)
	v_add_f32_e32 v226, v226, v223
	ds_bpermute_b32 v223, v207, v226
	s_waitcnt lgkmcnt(0)
	v_add_f32_e32 v226, v226, v223
	ds_bpermute_b32 v223, v208, v226
	s_waitcnt lgkmcnt(0)
	v_add_f32_e32 v226, v226, v223
	v_mov_b32_e32 v250, 0x358637bd
	v_fmamk_f32 v226, v226, 0x3a000000, v250
	v_cmp_gt_f32_e32 vcc, 0x800000, v226
	v_mul_f32_e32 v223, 0x4b800000, v226
	s_nop 1
	v_cndmask_b32_e32 v226, v226, v223, vcc
	v_rsq_f32_e32 v226, v226
	s_nop 0
	v_mul_f32_e32 v223, 0x45800000, v226
	v_mov_b32_e32 v250, 0x43e00000
	v_cndmask_b32_e32 v226, v226, v223, vcc
	s_waitcnt vmcnt(7)
	v_pk_mul_f32 v[40:41], v[40:41], v[226:227] op_sel_hi:[1,0]
	v_pk_mul_f32 v[42:43], v[42:43], v[226:227] op_sel_hi:[1,0]
	v_pk_add_f32 v[236:237], v[236:237], 1.0 op_sel_hi:[1,0]
	v_pk_add_f32 v[238:239], v[238:239], 1.0 op_sel_hi:[1,0]
	v_pk_mul_f32 v[40:41], v[228:229], v[40:41]
	v_pk_mul_f32 v[42:43], v[230:231], v[42:43]
	v_pk_fma_f32 v[40:41], v[236:237], v[40:41], v[232:233]
	v_pk_fma_f32 v[42:43], v[238:239], v[42:43], v[234:235]
	v_med3_f32 v228, v40, s13, v250
	v_med3_f32 v229, v41, s13, v250
	v_med3_f32 v230, v42, s13, v250
	v_med3_f32 v231, v43, s13, v250
	ds_write_b128 v35, v[40:43] offset:0
	v_cvt_pk_fp8_f32 v224, v228, v229
	v_cvt_pk_fp8_f32 v224, v230, v231 op_sel:[0,0,1]
	s_nop 0
	global_store_dword v33, v224, s[78:79] offset:0
	global_load_dwordx4 v[228:231], v27, s[100:101] offset:3072
	global_load_dwordx4 v[232:235], v27, s[82:83] offset:3072
	global_load_dwordx4 v[236:239], v27, s[98:99] offset:3072
	s_waitcnt vmcnt(8)
; #define LAS __attribute__((address_space(3)))
; DI unsigned pk_bf16(float lo, float hi) { f32x2 v = {lo, hi}; hbf16x2 r = __builtin_convertvector(v, hbf16x2); return __builtin_bit_cast(unsigned, r); }
; DI void phase_router(const Params& p, LAS unsigned char* lds, int G, int bid, const int layer, const float* xin_ctx, const float* xin_lat, const int row_lo, const int row_hi) {
;     ...
; #pragma unroll
;             for (int i = 0; i < 8; ++i) {
;                 const int col = 4 * lane + 256 * i;
;                 const f32x4 g = *(const f32x4*)(gain + col), sh = *(const f32x4*)(md + 3 * DM + col), scl = *(const f32x4*)(md + 4 * DM + col);
;                 const f32x4 hv = (v[i] * r * g) * (1.0f + scl) + sh;
;                 if (layer == 0 && !FP8_L0) { u32x2 w; w.x = pk_bf16(hv[0], hv[1]); w.y = pk_bf16(hv[2], hv[3]); *(u32x2*)(H + (size_t)row * DM + col) = w; }
;                 else *(unsigned*)(p.ws + WS_H8 + (size_t)row * DM + col) = pk_fp8x4(hv[0], hv[1], hv[2], hv[3]);
;                 *(LAS f32x4*)(hs + lr * RT_HS + col) = hv;
;             }
	v_pk_mul_f32 v[44:45], v[44:45], v[226:227] op_sel_hi:[1,0]
	v_pk_mul_f32 v[46:47], v[46:47], v[226:227] op_sel_hi:[1,0]
	v_pk_add_f32 v[216:217], v[216:217], 1.0 op_sel_hi:[1,0]
	v_pk_add_f32 v[218:219], v[218:219], 1.0 op_sel_hi:[1,0]
	v_pk_mul_f32 v[44:45], v[240:241], v[44:45]
	v_pk_mul_f32 v[46:47], v[242:243], v[46:47]
	v_pk_fma_f32 v[44:45], v[216:217], v[44:45], v[244:245]
	v_pk_fma_f32 v[46:47], v[218:219], v[46:47], v[246:247]
	v_med3_f32 v240, v44, s13, v250
	v_med3_f32 v241, v45, s13, v250
	v_med3_f32 v242, v46, s13, v250
	v_med3_f32 v243, v47, s13, v250
	ds_write_b128 v35, v[44:47] offset:1024
	v_cvt_pk_fp8_f32 v225, v240, v241
	v_cvt_pk_fp8_f32 v225, v242, v243 op_sel:[0,0,1]
	s_nop 0
	global_store_dword v33, v225, s[78:79] offset:256
	global_load_dwordx4 v[240:243], v29, s[100:101] offset:0
	global_load_dwordx4 v[244:247], v29, s[82:83] offset:0
	global_load_dwordx4 v[216:219], v29, s[98:99] offset:0
	s_waitcnt vmcnt(8)
	v_pk_mul_f32 v[48:49], v[48:49], v[226:227] op_sel_hi:[1,0]
	v_pk_mul_f32 v[50:51], v[50:51], v[226:227] op_sel_hi:[1,0]
	v_pk_add_f32 v[248:249], v[248:249], 1.0 op_sel_hi:[1,0]
	v_pk_add_f32 v[220:221], v[220:221], 1.0 op_sel_hi:[1,0]
	v_pk_mul_f32 v[48:49], v[2:3], v[48:49]
	v_pk_mul_f32 v[50:51], v[4:5], v[50:51]
	v_pk_fma_f32 v[48:49], v[248:249], v[48:49], v[6:7]
	v_pk_fma_f32 v[50:51], v[220:221], v[50:51], v[8:9]
	v_med3_f32 v2, v48, s13, v250
	v_med3_f32 v3, v49, s13, v250
	v_med3_f32 v4, v50, s13, v250
	v_med3_f32 v5, v51, s13, v250
	ds_write_b128 v35, v[48:51] offset:2048
	v_cvt_pk_fp8_f32 v215, v2, v3
	v_cvt_pk_fp8_f32 v215, v4, v5 op_sel:[0,0,1]
	s_nop 0
	global_store_dword v33, v215, s[78:79] offset:512
	global_load_dwordx4 v[2:5], v29, s[100:101] offset:1024
	global_load_dwordx4 v[6:9], v29, s[82:83] offset:1024
	global_load_dwordx2 v[248:249], v29, s[98:99] offset:1024
	global_load_dwordx2 v[220:221], v29, s[98:99] offset:1032
	s_waitcnt vmcnt(9)
	v_pk_mul_f32 v[52:53], v[52:53], v[226:227] op_sel_hi:[1,0]
	v_pk_mul_f32 v[54:55], v[54:55], v[226:227] op_sel_hi:[1,0]
	v_pk_add_f32 v[236:237], v[236:237], 1.0 op_sel_hi:[1,0]
	v_pk_add_f32 v[238:239], v[238:239], 1.0 op_sel_hi:[1,0]
	v_pk_mul_f32 v[52:53], v[228:229], v[52:53]
	v_pk_mul_f32 v[54:55], v[230:231], v[54:55]
	v_pk_fma_f32 v[52:53], v[236:237], v[52:53], v[232:233]
	v_pk_fma_f32 v[54:55], v[238:239], v[54:55], v[234:235]
	v_med3_f32 v228, v52, s13, v250
	v_med3_f32 v229, v53, s13, v250
	v_med3_f32 v230, v54, s13, v250
	v_med3_f32 v231, v55, s13, v250
	ds_write_b128 v35, v[52:55] offset:3072
	v_cvt_pk_fp8_f32 v224, v228, v229
	v_cvt_pk_fp8_f32 v224, v230, v231 op_sel:[0,0,1]
	s_nop 0
	global_store_dword v33, v224, s[78:79] offset:768
	global_load_dwordx4 v[228:231], v29, s[100:101] offset:2048
	global_load_dwordx4 v[232:235], v29, s[82:83] offset:2048
	global_load_dwordx4 v[236:239], v29, s[98:99] offset:2048
	s_waitcnt vmcnt(9)
	v_pk_mul_f32 v[56:57], v[56:57], v[226:227] op_sel_hi:[1,0]
	v_pk_mul_f32 v[58:59], v[58:59], v[226:227] op_sel_hi:[1,0]
	v_pk_add_f32 v[216:217], v[216:217], 1.0 op_sel_hi:[1,0]
	v_pk_add_f32 v[218:219], v[218:219], 1.0 op_sel_hi:[1,0]
	v_pk_mul_f32 v[56:57], v[240:241], v[56:57]
	v_pk_mul_f32 v[58:59], v[242:243], v[58:59]
	v_pk_fma_f32 v[56:57], v[216:217], v[56:57], v[244:245]
	v_pk_fma_f32 v[58:59], v[218:219], v[58:59], v[246:247]
	v_med3_f32 v240, v56, s13, v250
	v_med3_f32 v241, v57, s13, v250
	v_med3_f32 v242, v58, s13, v250
	v_med3_f32 v243, v59, s13, v250
	ds_write_b128 v35, v[56:59] offset:4096
	v_cvt_pk_fp8_f32 v225, v240, v241
	v_cvt_pk_fp8_f32 v225, v242, v243 op_sel:[0,0,1]
	s_nop 0
	global_store_dword v33, v225, s[78:79] offset:1024
	global_load_dwordx4 v[240:243], v29, s[100:101] offset:3072
	global_load_dwordx4 v[244:247], v29, s[82:83] offset:3072
	global_load_dwordx4 v[216:219], v29, s[98:99] offset:3072
	s_waitcnt vmcnt(8)
	v_pk_mul_f32 v[60:61], v[60:61], v[226:227] op_sel_hi:[1,0]
	v_pk_mul_f32 v[62:63], v[62:63], v[226:227] op_sel_hi:[1,0]
	v_pk_add_f32 v[248:249], v[248:249], 1.0 op_sel_hi:[1,0]
	v_pk_add_f32 v[220:221], v[220:221], 1.0 op_sel_hi:[1,0]
	v_pk_mul_f32 v[60:61], v[2:3], v[60:61]
	v_pk_mul_f32 v[62:63], v[4:5], v[62:63]
	v_pk_fma_f32 v[60:61], v[248:249], v[60:61], v[6:7]
	v_pk_fma_f32 v[62:63], v[220:221], v[62:63], v[8:9]
	v_med3_f32 v2, v60, s13, v250
	v_med3_f32 v3, v61, s13, v250
	v_med3_f32 v4, v62, s13, v250
	v_med3_f32 v5, v63, s13, v250
	ds_write_b128 v35, v[60:63] offset:5120
	v_cvt_pk_fp8_f32 v215, v2, v3
	v_cvt_pk_fp8_f32 v215, v4, v5 op_sel:[0,0,1]
	s_nop 0
	global_store_dword v33, v215, s[78:79] offset:1280
	s_waitcnt vmcnt(5)
	v_pk_mul_f32 v[64:65], v[64:65], v[226:227] op_sel_hi:[1,0]
	v_pk_mul_f32 v[66:67], v[66:67], v[226:227] op_sel_hi:[1,0]
	v_pk_add_f32 v[236:237], v[236:237], 1.0 op_sel_hi:[1,0]
	v_pk_add_f32 v[238:239], v[238:239], 1.0 op_sel_hi:[1,0]
	v_pk_mul_f32 v[64:65], v[228:229], v[64:65]
	v_pk_mul_f32 v[66:67], v[230:231], v[66:67]
	v_pk_fma_f32 v[64:65], v[236:237], v[64:65], v[232:233]
	v_pk_fma_f32 v[66:67], v[238:239], v[66:67], v[234:235]
	v_med3_f32 v228, v64, s13, v250
	v_med3_f32 v229, v65, s13, v250
	v_med3_f32 v230, v66, s13, v250
	v_med3_f32 v231, v67, s13, v250
	ds_write_b128 v35, v[64:67] offset:6144
	v_cvt_pk_fp8_f32 v224, v228, v229
	v_cvt_pk_fp8_f32 v224, v230, v231 op_sel:[0,0,1]
	s_nop 0
	global_store_dword v33, v224, s[78:79] offset:1536
	s_waitcnt vmcnt(2)
	v_pk_mul_f32 v[68:69], v[68:69], v[226:227] op_sel_hi:[1,0]
	v_pk_mul_f32 v[70:71], v[70:71], v[226:227] op_sel_hi:[1,0]
	v_pk_add_f32 v[216:217], v[216:217], 1.0 op_sel_hi:[1,0]
	v_pk_add_f32 v[218:219], v[218:219], 1.0 op_sel_hi:[1,0]
	v_pk_mul_f32 v[68:69], v[240:241], v[68:69]
	v_pk_mul_f32 v[70:71], v[242:243], v[70:71]
	v_pk_fma_f32 v[68:69], v[216:217], v[68:69], v[244:245]
	v_pk_fma_f32 v[70:71], v[218:219], v[70:71], v[246:247]
	v_med3_f32 v240, v68, s13, v250
	v_med3_f32 v241, v69, s13, v250
	v_med3_f32 v242, v70, s13, v250
	v_med3_f32 v243, v71, s13, v250
	ds_write_b128 v35, v[68:71] offset:7168
	v_cvt_pk_fp8_f32 v225, v240, v241
	v_cvt_pk_fp8_f32 v225, v242, v243 op_sel:[0,0,1]
	s_nop 0
	global_store_dword v33, v225, s[78:79] offset:1792
	s_branch .LBB0_743

; DI float bflo(unsigned w) { return __uint_as_float(w << 16); }
; DI float bfhi(unsigned w) { return __uint_as_float(w & 0xffff0000u); }
; template <bool FINAL>
; DI void phase_combine(const Params& p, LAS unsigned char* lds, int G, int bid, const int layer, const float* xin_ctx, const float* xin_lat, const int row_lo, const int row_hi) {
;     ...
;     for (int row = row_lo + bid * 8 + wave; row < row_hi; row += G * 8) {
;         const TokInfo ti = TOK[row];
;         const bf16_t* o0 = OUT2 + (size_t)(MT[ti.e0] + ti.p0) * DM; const bf16_t* o1 = OUT2 + (size_t)(MT[ti.e1] + ti.p1) * DM;
;         const float* xr = row < NCTX ? xin_ctx + (size_t)row * DM : xin_lat + (size_t)(row - NCTX) * DM;
;         const bf16_t* dr = (const bf16_t*)(p.ws + WS_D) + (size_t)row * DM;
;         const int mi = row_mod(row);
;         const float* g1 = MOD + ((size_t)layer * 5 + mi) * MODN + 2 * DM;
;         const float* g2 = MOD + ((size_t)layer * 5 + mi) * MODN + 5 * DM;
;         f32x4 v[8];
; #pragma unroll
;         for (int i = 0; i < 8; ++i) {
;             const int col = 4 * lane + 256 * i;
;             const u32x2 dw = *(const u32x2*)(dr + col);
;             const f32x4 x = *(const f32x4*)(xr + col) + *(const f32x4*)(g1 + col) * (f32x4){bflo(dw.x), bfhi(dw.x), bflo(dw.y), bfhi(dw.y)}, g = *(const f32x4*)(g2 + col);
;             const u32x2 a = *(const u32x2*)(o0 + col), b = *(const u32x2*)(o1 + col);
;             const f32x4 fa = {bflo(a.x), bfhi(a.x), bflo(a.y), bfhi(a.y)}, fb = {bflo(b.x), bfhi(b.x), bflo(b.y), bfhi(b.y)};
;             v[i] = x + g * (fa * ti.w0 + fb * ti.w1);
;         }
.LBB0_1124:
	v_lshl_add_u64 v[6:7], s[50:51], 0, v[52:53]
	v_add_co_u32_e32 v2, vcc, 0x32d2e000, v6
	v_cmp_lt_i32_e64 s[0:1], s56, v34
	s_nop 0
	v_addc_co_u32_e32 v3, vcc, 0, v7, vcc
	global_load_dwordx4 v[2:5], v[2:3], off
	v_lshl_add_u64 v[6:7], v[6:7], 0, s[18:19]
	global_load_dwordx2 v[76:77], v[6:7], off offset:16
	v_cmp_gt_i32_e32 vcc, s27, v34
	v_add_u32_e32 v38, 0xfffffc00, v34
	s_waitcnt vmcnt(1)
	v_lshl_add_u32 v2, v2, 2, s7
	v_lshl_add_u32 v6, v4, 2, s7
	ds_read_b32 v4, v2
	ds_read_b32 v2, v6
	s_and_saveexec_b64 s[70:71], s[0:1]
	s_xor_b64 s[0:1], exec, s[70:71]
	v_add_u32_e32 v38, 0xfffffc00, v34
	v_lshlrev_b64 v[6:7], 13, v[38:39]
	v_lshl_add_u64 v[22:23], s[52:53], 0, v[6:7]
	s_andn2_saveexec_b64 s[0:1], s[0:1]
	v_mov_b64_e32 v[22:23], v[56:57]
	s_or_b64 exec, exec, s[0:1]
	s_waitcnt lgkmcnt(1)
	v_add_u32_e32 v6, v4, v3
	v_ashrrev_i32_e32 v7, 31, v6
	s_waitcnt lgkmcnt(0)
	v_add_u32_e32 v2, v2, v5
	v_lshl_add_u64 v[8:9], s[50:51], 0, v[60:61]
	v_lshlrev_b64 v[6:7], 12, v[6:7]
	v_ashrrev_i32_e32 v3, 31, v2
	v_lshrrev_b32_e32 v4, 11, v38
	v_add_co_u32_e64 v24, s[0:1], s58, v8
	v_lshlrev_b64 v[2:3], 12, v[2:3]
	v_lshl_add_u64 v[26:27], v[50:51], 0, v[6:7]
	v_cndmask_b32_e64 v6, v4, 4, vcc
	v_mov_b64_e32 v[4:5], s[4:5]
	v_addc_co_u32_e64 v25, s[0:1], 0, v9, s[0:1]
	v_lshl_add_u64 v[28:29], v[50:51], 0, v[2:3]
	v_mad_u64_u32 v[78:79], s[0:1], v6, s57, v[4:5]
	global_load_dwordx2 v[114:115], v[24:25], off nt
	global_load_dwordx2 v[116:117], v[24:25], off offset:512 nt
	global_load_dwordx2 v[118:119], v[26:27], off nt
	global_load_dwordx2 v[122:123], v[26:27], off offset:512 nt
	global_load_dwordx2 v[120:121], v[28:29], off nt
	v_lshl_add_u64 v[30:31], v[78:79], 0, s[30:31]
	v_lshlrev_b32_e32 v38, 2, v36
	v_lshl_add_u64 v[2:3], v[30:31], 0, v[38:39]
	v_mov_b32_e32 v63, v39
	v_lshl_add_u64 v[82:83], v[78:79], 0, s[34:35]
	v_lshl_add_u64 v[18:19], v[22:23], 0, v[38:39]
	global_load_dwordx2 v[124:125], v[28:29], off offset:512 nt
	s_nop 0
	global_load_dwordx4 v[2:5], v[2:3], off
	s_nop 0
	global_load_dwordx4 v[6:9], v[18:19], off
	global_load_dwordx4 v[10:13], v[18:19], off offset:1024
	v_lshl_add_u64 v[14:15], v[30:31], 0, v[62:63]
	v_lshl_add_u64 v[20:21], v[82:83], 0, v[38:39]
	global_load_dwordx4 v[14:17], v[14:15], off
	v_mov_b32_e32 v65, v39
	global_load_dwordx4 v[90:93], v[20:21], off
	v_lshl_add_u64 v[20:21], v[82:83], 0, v[62:63]
	global_load_dwordx4 v[94:97], v[20:21], off
	global_load_dwordx2 v[126:127], v[24:25], off offset:1024 nt
	v_lshl_add_u64 v[20:21], v[30:31], 0, v[64:65]
	global_load_dwordx4 v[98:101], v[18:19], off offset:2048
	global_load_dwordx4 v[102:105], v[20:21], off
	global_load_dwordx2 v[128:129], v[26:27], off offset:1024 nt
	global_load_dwordx2 v[130:131], v[28:29], off offset:1024 nt
	v_mov_b32_e32 v67, v39
	v_lshl_add_u64 v[106:107], v[82:83], 0, v[64:65]
	v_lshl_add_u64 v[110:111], v[30:31], 0, v[66:67]
	global_load_dwordx2 v[132:133], v[24:25], off offset:1536 nt
	s_nop 0
	global_load_dwordx4 v[18:21], v[18:19], off offset:3072
	s_nop 0
	global_load_dwordx2 v[84:85], v[26:27], off offset:1536 nt
	global_load_dwordx2 v[32:33], v[28:29], off offset:1536 nt
	s_nop 0
	global_load_dwordx4 v[106:109], v[106:107], off
	s_nop 0
	global_load_dwordx4 v[110:113], v[110:111], off
	s_waitcnt vmcnt(23)
	v_mov_b32_e32 v80, v77
	v_mov_b32_e32 v69, v39
	v_mov_b32_e32 v71, v39
	v_mov_b32_e32 v73, v39
	v_mov_b32_e32 v75, v39
	v_cmp_lt_i32_e32 vcc, s56, v34
	s_waitcnt vmcnt(22)
	v_lshlrev_b32_e32 v134, 16, v114
	v_and_b32_e32 v135, 0xffff0000, v114
	v_lshlrev_b32_e32 v114, 16, v115
	v_and_b32_e32 v115, 0xffff0000, v115
	s_waitcnt vmcnt(18)
	v_lshlrev_b32_e32 v140, 16, v120
	v_and_b32_e32 v141, 0xffff0000, v120
	v_lshlrev_b32_e32 v120, 16, v121
	v_and_b32_e32 v121, 0xffff0000, v121
	v_lshlrev_b32_e32 v138, 16, v118
	v_and_b32_e32 v139, 0xffff0000, v118
	v_lshlrev_b32_e32 v118, 16, v119
	v_and_b32_e32 v119, 0xffff0000, v119
	s_waitcnt vmcnt(15)
	v_pk_fma_f32 v[2:3], v[2:3], v[134:135], v[6:7]
	v_pk_mul_f32 v[6:7], v[80:81], v[120:121] op_sel_hi:[0,1]
	v_lshlrev_b32_e32 v136, 16, v116
	v_and_b32_e32 v137, 0xffff0000, v116
	v_lshlrev_b32_e32 v144, 16, v124
	v_and_b32_e32 v145, 0xffff0000, v124
	v_pk_fma_f32 v[4:5], v[4:5], v[114:115], v[8:9]
	v_pk_mul_f32 v[8:9], v[80:81], v[140:141] op_sel_hi:[0,1]
	v_pk_fma_f32 v[6:7], v[76:77], v[118:119], v[6:7] op_sel_hi:[0,1,1]
	v_lshlrev_b32_e32 v142, 16, v122
	v_and_b32_e32 v143, 0xffff0000, v122
	s_waitcnt vmcnt(13)
	v_pk_fma_f32 v[10:11], v[14:15], v[136:137], v[10:11]
	v_pk_fma_f32 v[14:15], v[76:77], v[138:139], v[8:9] op_sel_hi:[0,1,1]
	s_waitcnt vmcnt(12)
	v_pk_fma_f32 v[8:9], v[92:93], v[6:7], v[4:5]
	v_pk_mul_f32 v[4:5], v[80:81], v[144:145] op_sel_hi:[0,1]
	v_lshlrev_b32_e32 v116, 16, v117
	v_and_b32_e32 v117, 0xffff0000, v117
	v_pk_fma_f32 v[118:119], v[76:77], v[142:143], v[4:5] op_sel_hi:[0,1,1]
	v_lshl_add_u64 v[4:5], v[82:83], 0, v[66:67]
	v_pk_fma_f32 v[12:13], v[16:17], v[116:117], v[12:13]
	v_pk_fma_f32 v[6:7], v[90:91], v[14:15], v[2:3]
	global_load_dwordx4 v[14:17], v[4:5], off
	global_load_dwordx2 v[136:137], v[26:27], off offset:2048 nt
	v_lshlrev_b32_e32 v2, 16, v125
	v_and_b32_e32 v3, 0xffff0000, v125
	v_lshlrev_b32_e32 v122, 16, v123
	v_and_b32_e32 v123, 0xffff0000, v123
	v_pk_mul_f32 v[2:3], v[80:81], v[2:3] op_sel_hi:[0,1]
	v_pk_fma_f32 v[2:3], v[76:77], v[122:123], v[2:3] op_sel_hi:[0,1,1]
	s_waitcnt vmcnt(13)
	v_pk_fma_f32 v[4:5], v[96:97], v[2:3], v[12:13]
	v_lshl_add_u64 v[2:3], v[22:23], 0, v[68:69]
	global_load_dwordx4 v[90:93], v[2:3], off
	v_lshl_add_u64 v[2:3], v[30:31], 0, v[68:69]
	s_waitcnt vmcnt(9)
; DI float bflo(unsigned w) { return __uint_as_float(w << 16); }
; DI float bfhi(unsigned w) { return __uint_as_float(w & 0xffff0000u); }
; template <bool FINAL>
; DI void phase_combine(const Params& p, LAS unsigned char* lds, int G, int bid, const int layer, const float* xin_ctx, const float* xin_lat, const int row_lo, const int row_hi) {
;     ...
; #pragma unroll
;         for (int i = 0; i < 8; ++i) {
;             const int col = 4 * lane + 256 * i;
;             const u32x2 dw = *(const u32x2*)(dr + col);
;             const f32x4 x = *(const f32x4*)(xr + col) + *(const f32x4*)(g1 + col) * (f32x4){bflo(dw.x), bfhi(dw.x), bflo(dw.y), bfhi(dw.y)}, g = *(const f32x4*)(g2 + col);
;             const u32x2 a = *(const u32x2*)(o0 + col), b = *(const u32x2*)(o1 + col);
;             const f32x4 fa = {bflo(a.x), bfhi(a.x), bflo(a.y), bfhi(a.y)}, fb = {bflo(b.x), bfhi(b.x), bflo(b.y), bfhi(b.y)};
;             v[i] = x + g * (fa * ti.w0 + fb * ti.w1);
	v_lshlrev_b32_e32 v122, 16, v130
	v_and_b32_e32 v123, 0xffff0000, v130
	v_lshlrev_b32_e32 v124, 16, v131
	v_and_b32_e32 v125, 0xffff0000, v131
	global_load_dwordx2 v[134:135], v[24:25], off offset:2048 nt
	global_load_dwordx4 v[114:117], v[2:3], off
	v_pk_fma_f32 v[2:3], v[94:95], v[118:119], v[10:11]
	v_lshlrev_b32_e32 v12, 16, v127
	v_and_b32_e32 v13, 0xffff0000, v127
	v_lshlrev_b32_e32 v118, 16, v128
	v_and_b32_e32 v119, 0xffff0000, v128
	v_lshlrev_b32_e32 v120, 16, v129
	v_and_b32_e32 v121, 0xffff0000, v129
	v_pk_mul_f32 v[124:125], v[80:81], v[124:125] op_sel_hi:[0,1]
	v_pk_mul_f32 v[122:123], v[80:81], v[122:123] op_sel_hi:[0,1]
	v_lshlrev_b32_e32 v10, 16, v126
	v_and_b32_e32 v11, 0xffff0000, v126
	global_load_dwordx2 v[138:139], v[28:29], off offset:2048 nt
	v_pk_fma_f32 v[12:13], v[104:105], v[12:13], v[100:101]
	v_pk_fma_f32 v[130:131], v[76:77], v[118:119], v[122:123] op_sel_hi:[0,1,1]
	v_pk_fma_f32 v[118:119], v[76:77], v[120:121], v[124:125] op_sel_hi:[0,1,1]
	v_pk_fma_f32 v[10:11], v[102:103], v[10:11], v[98:99]
	v_lshl_add_u64 v[94:95], v[82:83], 0, v[68:69]
	v_lshl_add_u64 v[98:99], v[22:23], 0, v[70:71]
	v_lshl_add_u64 v[102:103], v[30:31], 0, v[70:71]
	s_waitcnt vmcnt(7)
	v_pk_fma_f32 v[12:13], v[108:109], v[118:119], v[12:13]
	v_lshl_add_u64 v[108:109], v[82:83], 0, v[70:71]
	global_load_dwordx4 v[94:97], v[94:95], off
	s_nop 0
	global_load_dwordx2 v[140:141], v[24:25], off offset:2560 nt
	global_load_dwordx2 v[142:143], v[26:27], off offset:2560 nt
	global_load_dwordx2 v[144:145], v[28:29], off offset:2560 nt
	v_pk_fma_f32 v[10:11], v[106:107], v[130:131], v[10:11]
	global_load_dwordx4 v[98:101], v[98:99], off
	v_lshlrev_b32_e32 v106, 16, v132
	global_load_dwordx4 v[102:105], v[102:103], off
	s_nop 0
	global_load_dwordx4 v[118:121], v[108:109], off
	global_load_dwordx2 v[146:147], v[24:25], off offset:3072 nt
	v_lshl_add_u64 v[108:109], v[22:23], 0, v[72:73]
	global_load_dwordx4 v[122:125], v[108:109], off
	v_lshl_add_u64 v[108:109], v[30:31], 0, v[72:73]
	v_and_b32_e32 v107, 0xffff0000, v132
	global_load_dwordx4 v[126:129], v[108:109], off
	global_load_dwordx2 v[130:131], v[26:27], off offset:3072 nt
	global_load_dwordx2 v[148:149], v[28:29], off offset:3072 nt
	v_lshlrev_b32_e32 v108, 16, v133
	v_and_b32_e32 v109, 0xffff0000, v133
	s_waitcnt vmcnt(18)
	v_pk_fma_f32 v[150:151], v[110:111], v[106:107], v[18:19]
	v_lshl_add_u64 v[18:19], v[82:83], 0, v[72:73]
	v_lshl_add_u64 v[22:23], v[22:23], 0, v[74:75]
	v_pk_fma_f32 v[132:133], v[112:113], v[108:109], v[20:21]
	global_load_dwordx4 v[18:21], v[18:19], off
	s_nop 0
	global_load_dwordx2 v[154:155], v[24:25], off offset:3584 nt
	global_load_dwordx4 v[106:109], v[22:23], off
	v_lshl_add_u64 v[22:23], v[30:31], 0, v[74:75]
	v_lshlrev_b32_e32 v24, 16, v33
	v_and_b32_e32 v25, 0xffff0000, v33
	v_lshlrev_b32_e32 v152, 16, v84
	v_and_b32_e32 v153, 0xffff0000, v84
	v_lshlrev_b32_e32 v84, 16, v85
	global_load_dwordx4 v[110:113], v[22:23], off
	global_load_dwordx2 v[158:159], v[28:29], off offset:3584 nt
	v_and_b32_e32 v85, 0xffff0000, v85
	v_pk_mul_f32 v[24:25], v[80:81], v[24:25] op_sel_hi:[0,1]
	global_load_dwordx2 v[156:157], v[26:27], off offset:3584 nt
	v_pk_fma_f32 v[24:25], v[76:77], v[84:85], v[24:25] op_sel_hi:[0,1,1]
	v_lshlrev_b32_e32 v22, 16, v32
	v_and_b32_e32 v23, 0xffff0000, v32
	v_pk_mul_f32 v[22:23], v[80:81], v[22:23] op_sel_hi:[0,1]
	v_pk_fma_f32 v[22:23], v[76:77], v[152:153], v[22:23] op_sel_hi:[0,1,1]
	s_waitcnt vmcnt(23)
	v_pk_fma_f32 v[32:33], v[16:17], v[24:25], v[132:133]
	v_lshl_add_u64 v[16:17], v[82:83], 0, v[74:75]
	global_load_dwordx4 v[82:85], v[16:17], off
	v_pk_fma_f32 v[30:31], v[14:15], v[22:23], v[150:151]
	s_waitcnt vmcnt(23)
	v_lshlrev_b32_e32 v22, 16, v136
	v_and_b32_e32 v23, 0xffff0000, v136
	v_lshlrev_b32_e32 v24, 16, v137
	v_and_b32_e32 v25, 0xffff0000, v137
	s_waitcnt vmcnt(21)
	v_lshlrev_b32_e32 v14, 16, v134
	v_and_b32_e32 v15, 0xffff0000, v134
	v_lshlrev_b32_e32 v16, 16, v135
	v_and_b32_e32 v17, 0xffff0000, v135
	s_waitcnt vmcnt(20)
	v_pk_fma_f32 v[16:17], v[116:117], v[16:17], v[92:93]
	v_pk_fma_f32 v[14:15], v[114:115], v[14:15], v[90:91]
	s_waitcnt vmcnt(19)
; DI float bflo(unsigned w) { return __uint_as_float(w << 16); }
; DI float bfhi(unsigned w) { return __uint_as_float(w & 0xffff0000u); }
; template <bool FINAL>
; DI void phase_combine(const Params& p, LAS unsigned char* lds, int G, int bid, const int layer, const float* xin_ctx, const float* xin_lat, const int row_lo, const int row_hi) {
;     ...
;             const f32x4 x = *(const f32x4*)(xr + col) + *(const f32x4*)(g1 + col) * (f32x4){bflo(dw.x), bfhi(dw.x), bflo(dw.y), bfhi(dw.y)}, g = *(const f32x4*)(g2 + col);
;             const u32x2 a = *(const u32x2*)(o0 + col), b = *(const u32x2*)(o1 + col);
;             const f32x4 fa = {bflo(a.x), bfhi(a.x), bflo(a.y), bfhi(a.y)}, fb = {bflo(b.x), bfhi(b.x), bflo(b.y), bfhi(b.y)};
;             v[i] = x + g * (fa * ti.w0 + fb * ti.w1);
;         }
;         if (!FINAL) {
;             if (row >= NCTX)
; #pragma unroll
;             for (int i = 0; i < 8; ++i) *(f32x4*)(XB + (size_t)row * DM + 4 * lane + 256 * i) = v[i];
	v_lshlrev_b32_e32 v26, 16, v138
	v_and_b32_e32 v27, 0xffff0000, v138
	v_lshlrev_b32_e32 v28, 16, v139
	v_and_b32_e32 v29, 0xffff0000, v139
	v_pk_mul_f32 v[28:29], v[80:81], v[28:29] op_sel_hi:[0,1]
	v_pk_mul_f32 v[26:27], v[80:81], v[26:27] op_sel_hi:[0,1]
	v_pk_fma_f32 v[22:23], v[76:77], v[22:23], v[26:27] op_sel_hi:[0,1,1]
	v_pk_fma_f32 v[24:25], v[76:77], v[24:25], v[28:29] op_sel_hi:[0,1,1]
	s_waitcnt vmcnt(18)
	v_pk_fma_f32 v[28:29], v[96:97], v[24:25], v[16:17]
	v_pk_fma_f32 v[26:27], v[94:95], v[22:23], v[14:15]
	s_waitcnt vmcnt(17)
	v_lshlrev_b32_e32 v14, 16, v140
	s_waitcnt vmcnt(15)
	v_lshlrev_b32_e32 v90, 16, v144
	v_and_b32_e32 v91, 0xffff0000, v144
	v_lshlrev_b32_e32 v92, 16, v145
	v_and_b32_e32 v93, 0xffff0000, v145
	v_and_b32_e32 v15, 0xffff0000, v140
	v_lshlrev_b32_e32 v16, 16, v141
	v_and_b32_e32 v17, 0xffff0000, v141
	v_lshlrev_b32_e32 v22, 16, v142
	v_and_b32_e32 v23, 0xffff0000, v142
	v_lshlrev_b32_e32 v24, 16, v143
	v_and_b32_e32 v25, 0xffff0000, v143
	v_pk_mul_f32 v[92:93], v[80:81], v[92:93] op_sel_hi:[0,1]
	v_pk_mul_f32 v[90:91], v[80:81], v[90:91] op_sel_hi:[0,1]
	s_waitcnt vmcnt(13)
	v_pk_fma_f32 v[16:17], v[104:105], v[16:17], v[100:101]
	v_pk_fma_f32 v[14:15], v[102:103], v[14:15], v[98:99]
	v_pk_fma_f32 v[22:23], v[76:77], v[22:23], v[90:91] op_sel_hi:[0,1,1]
	v_pk_fma_f32 v[24:25], v[76:77], v[24:25], v[92:93] op_sel_hi:[0,1,1]
	s_waitcnt vmcnt(7)
	v_lshlrev_b32_e32 v94, 16, v148
	v_and_b32_e32 v95, 0xffff0000, v148
	v_lshlrev_b32_e32 v96, 16, v149
	v_and_b32_e32 v97, 0xffff0000, v149
	v_pk_fma_f32 v[24:25], v[120:121], v[24:25], v[16:17]
	v_pk_fma_f32 v[22:23], v[118:119], v[22:23], v[14:15]
	v_lshlrev_b32_e32 v14, 16, v146
	v_and_b32_e32 v15, 0xffff0000, v146
	v_lshlrev_b32_e32 v16, 16, v147
	v_and_b32_e32 v17, 0xffff0000, v147
	v_lshlrev_b32_e32 v90, 16, v130
	v_and_b32_e32 v91, 0xffff0000, v130
	v_lshlrev_b32_e32 v92, 16, v131
	v_and_b32_e32 v93, 0xffff0000, v131
	v_pk_mul_f32 v[96:97], v[80:81], v[96:97] op_sel_hi:[0,1]
	v_pk_mul_f32 v[94:95], v[80:81], v[94:95] op_sel_hi:[0,1]
	v_pk_fma_f32 v[16:17], v[128:129], v[16:17], v[124:125]
	v_pk_fma_f32 v[14:15], v[126:127], v[14:15], v[122:123]
	v_pk_fma_f32 v[90:91], v[76:77], v[90:91], v[94:95] op_sel_hi:[0,1,1]
	v_pk_fma_f32 v[92:93], v[76:77], v[92:93], v[96:97] op_sel_hi:[0,1,1]
	s_waitcnt vmcnt(2)
	v_lshlrev_b32_e32 v94, 16, v158
	v_and_b32_e32 v95, 0xffff0000, v158
	v_lshlrev_b32_e32 v96, 16, v159
	v_and_b32_e32 v97, 0xffff0000, v159
	v_pk_fma_f32 v[20:21], v[20:21], v[92:93], v[16:17]
	v_pk_fma_f32 v[18:19], v[18:19], v[90:91], v[14:15]
	v_lshlrev_b32_e32 v14, 16, v154
	v_and_b32_e32 v15, 0xffff0000, v154
	v_lshlrev_b32_e32 v16, 16, v155
	v_and_b32_e32 v17, 0xffff0000, v155
	s_waitcnt vmcnt(1)
	v_lshlrev_b32_e32 v90, 16, v156
	v_and_b32_e32 v91, 0xffff0000, v156
	v_lshlrev_b32_e32 v92, 16, v157
	v_and_b32_e32 v93, 0xffff0000, v157
	v_pk_mul_f32 v[96:97], v[80:81], v[96:97] op_sel_hi:[0,1]
	v_pk_mul_f32 v[94:95], v[80:81], v[94:95] op_sel_hi:[0,1]
	v_pk_fma_f32 v[16:17], v[112:113], v[16:17], v[108:109]
	v_pk_fma_f32 v[14:15], v[110:111], v[14:15], v[106:107]
	v_pk_fma_f32 v[90:91], v[76:77], v[90:91], v[94:95] op_sel_hi:[0,1,1]
	v_pk_fma_f32 v[76:77], v[76:77], v[92:93], v[96:97] op_sel_hi:[0,1,1]
	s_waitcnt vmcnt(0)
	v_pk_fma_f32 v[16:17], v[84:85], v[76:77], v[16:17]
	v_pk_fma_f32 v[14:15], v[82:83], v[90:91], v[14:15]
	s_and_saveexec_b64 s[0:1], vcc
	s_cbranch_execz .LBB0_1123
	v_lshl_add_u64 v[76:77], s[50:51], 0, v[54:55]
	v_add_co_u32_e32 v82, vcc, 0x1fa0e000, v76
	s_nop 1
	v_addc_co_u32_e32 v83, vcc, 0, v77, vcc
	v_add_co_u32_e32 v76, vcc, 0x1fa0f000, v76
	global_store_dwordx4 v[82:83], v[6:9], off
	global_store_dwordx4 v[82:83], v[2:5], off offset:1024
	global_store_dwordx4 v[82:83], v[10:13], off offset:2048
	global_store_dwordx4 v[82:83], v[30:33], off offset:3072
	v_addc_co_u32_e32 v77, vcc, 0, v77, vcc
	global_store_dwordx4 v[76:77], v[26:29], off
	global_store_dwordx4 v[76:77], v[22:25], off offset:1024
	global_store_dwordx4 v[76:77], v[18:21], off offset:2048
	global_store_dwordx4 v[76:77], v[14:17], off offset:3072
	s_branch .LBB0_1123

; DI float bflo(unsigned w) { return __uint_as_float(w << 16); }
; DI float bfhi(unsigned w) { return __uint_as_float(w & 0xffff0000u); }
; DI void phase_router(const Params& p, LAS unsigned char* lds, int G, int bid, const int layer, const float* xin_ctx, const float* xin_lat, const int row_lo, const int row_hi) {
;     ...
;         for (int rr = 0; rr < 2; ++rr) {
;             const int lr = 2 * wave + rr, row = row_lo + bt * 16 + lr;
;             const float* xr = row < NCTX ? xin_ctx + (size_t)row * DM : xin_lat + (size_t)(row - NCTX) * DM;
;             const bf16_t* dr = (const bf16_t*)(p.ws + WS_D) + (size_t)row * DM;
;             const float* md = MOD + (size_t)row_mod(row) * MODN;
;             f32x4 v[8]; float ss = 0.f;
; #pragma unroll
;             for (int i = 0; i < 8; ++i) {
;                 const int col = 4 * lane + 256 * i;
;                 const u32x2 dw = *(const u32x2*)(dr + col);
;                 v[i] = *(const f32x4*)(xr + col) + *(const f32x4*)(md + 2 * DM + col) * (f32x4){bflo(dw.x), bfhi(dw.x), bflo(dw.y), bfhi(dw.y)};
;                 ss += v[i][0] * v[i][0] + v[i][1] * v[i][1] + v[i][2] * v[i][2] + v[i][3] * v[i][3];
;             }
.Lrt14_rows:
	v_readlane_b32 s100, v251, 12
	v_readlane_b32 s101, v251, 13
	v_readfirstlane_b32 s41, v0
	v_and_b32_e32 v33, 63, v0
	v_lshlrev_b32_e32 v27, 4, v33
	v_lshlrev_b32_e32 v31, 3, v33
	v_lshlrev_b32_e32 v33, 2, v33
	v_add_u32_e32 v29, 0x1000, v27
	s_lshr_b32 s41, s41, 6
	s_mov_b32 s17, 0xc3e00000
	s_lshl_b32 s53, s41, 1
	s_add_i32 s52, s40, s53
	s_mul_i32 s53, s53, 0x2010
	v_add_u32_e32 v35, s53, v27
	s_lshl_b32 s16, s52, 13
	s_add_u32 s72, s50, s16
	s_addc_u32 s73, s51, 0
	s_add_u32 s72, s72, 0x1fa0e000
	s_addc_u32 s73, s73, 0
	s_lshl_b32 s16, s52, 12
	s_add_u32 s74, s50, s16
	s_addc_u32 s75, s51, 0
	s_add_u32 s74, s74, 0x3af76000
	s_addc_u32 s75, s75, 0
	s_lshl_b32 s16, s52, 11
	s_add_u32 s76, s50, s16
	s_addc_u32 s77, s51, 0
	s_add_u32 s76, s76, 0x41b76000
	s_addc_u32 s77, s77, 0
	s_sub_i32 s16, s52, 0x400
	s_lshr_b32 s16, s16, 11
	s_cmp_lt_u32 s52, 0x400
	s_cselect_b32 s16, 4, s16
	s_mul_i32 s16, s16, 0xc000
	s_add_u32 s78, s50, s16
	s_addc_u32 s79, s51, 0
	s_add_u32 s78, s78, 0x50000
	s_addc_u32 s79, s79, 0
	s_add_u32 s82, s78, 0x2000
	s_addc_u32 s83, s79, 0
	s_add_u32 s98, s78, 0x4000
	s_addc_u32 s99, s79, 0
	global_load_dwordx2 v[2:3], v31, s[74:75] offset:0 nt
	global_load_dwordx4 v[40:43], v27, s[72:73] offset:0 nt
	global_load_dwordx4 v[228:231], v27, s[78:79] offset:0
	global_load_dwordx2 v[4:5], v31, s[74:75] offset:512 nt
	global_load_dwordx4 v[44:47], v27, s[72:73] offset:1024 nt
	global_load_dwordx4 v[232:235], v27, s[78:79] offset:1024
	global_load_dwordx2 v[6:7], v31, s[74:75] offset:1024 nt
	global_load_dwordx4 v[48:51], v27, s[72:73] offset:2048 nt
	global_load_dwordx4 v[236:239], v27, s[78:79] offset:2048
	global_load_dwordx2 v[8:9], v31, s[74:75] offset:1536 nt
	global_load_dwordx4 v[52:55], v27, s[72:73] offset:3072 nt
	global_load_dwordx4 v[240:243], v27, s[78:79] offset:3072
	global_load_dwordx2 v[216:217], v31, s[74:75] offset:2048 nt
	global_load_dwordx4 v[56:59], v29, s[72:73] offset:0 nt
	global_load_dwordx4 v[244:247], v29, s[78:79] offset:0
	global_load_dwordx2 v[218:219], v31, s[74:75] offset:2560 nt
	global_load_dwordx4 v[60:63], v29, s[72:73] offset:1024 nt
	global_load_dwordx2 v[220:221], v31, s[74:75] offset:3072 nt
	global_load_dwordx4 v[64:67], v29, s[72:73] offset:2048 nt
	global_load_dwordx2 v[224:225], v31, s[74:75] offset:3584 nt
	global_load_dwordx4 v[68:71], v29, s[72:73] offset:3072 nt
	s_waitcnt vmcnt(18)
	v_and_b32_e32 v223, 0xffff0000, v2
	v_and_b32_e32 v250, 0xffff0000, v3
	v_lshlrev_b32_e32 v2, 16, v2
	v_lshlrev_b32_e32 v3, 16, v3
	v_fmac_f32_e32 v40, v228, v2
	v_fmac_f32_e32 v41, v229, v223
	v_fmac_f32_e32 v42, v230, v3
	v_fmac_f32_e32 v43, v231, v250
	global_load_dwordx4 v[228:231], v29, s[78:79] offset:1024
	v_mul_f32_e32 v226, v41, v41
	v_fmac_f32_e32 v226, v40, v40
	v_fmac_f32_e32 v226, v42, v42
	v_fmac_f32_e32 v226, v43, v43
	s_waitcnt vmcnt(16)
	v_and_b32_e32 v223, 0xffff0000, v4
	v_and_b32_e32 v250, 0xffff0000, v5
	v_lshlrev_b32_e32 v4, 16, v4
	v_lshlrev_b32_e32 v5, 16, v5
	v_fmac_f32_e32 v44, v232, v4
	v_fmac_f32_e32 v45, v233, v223
	v_fmac_f32_e32 v46, v234, v5
	v_fmac_f32_e32 v47, v235, v250
	global_load_dwordx4 v[232:235], v29, s[78:79] offset:2048
	v_mul_f32_e32 v223, v45, v45
	v_fmac_f32_e32 v223, v44, v44
	v_fmac_f32_e32 v223, v46, v46
	v_fmac_f32_e32 v223, v47, v47
	v_add_f32_e32 v226, v226, v223
	s_waitcnt vmcnt(14)
	v_and_b32_e32 v223, 0xffff0000, v6
	v_and_b32_e32 v250, 0xffff0000, v7
	v_lshlrev_b32_e32 v6, 16, v6
	v_lshlrev_b32_e32 v7, 16, v7
	v_fmac_f32_e32 v48, v236, v6
	v_fmac_f32_e32 v49, v237, v223
	v_fmac_f32_e32 v50, v238, v7
	v_fmac_f32_e32 v51, v239, v250
	global_load_dwordx4 v[236:239], v29, s[78:79] offset:3072
	v_mul_f32_e32 v223, v49, v49
	v_fmac_f32_e32 v223, v48, v48
	v_fmac_f32_e32 v223, v50, v50
	v_fmac_f32_e32 v223, v51, v51
	v_add_f32_e32 v226, v226, v223
	s_waitcnt vmcnt(12)
	v_and_b32_e32 v223, 0xffff0000, v8
	v_and_b32_e32 v250, 0xffff0000, v9
	v_lshlrev_b32_e32 v8, 16, v8
	v_lshlrev_b32_e32 v9, 16, v9
	v_fmac_f32_e32 v52, v240, v8
	v_fmac_f32_e32 v53, v241, v223
	v_fmac_f32_e32 v54, v242, v9
	v_fmac_f32_e32 v55, v243, v250
	v_mul_f32_e32 v223, v53, v53
	v_fmac_f32_e32 v223, v52, v52
	v_fmac_f32_e32 v223, v54, v54
	v_fmac_f32_e32 v223, v55, v55
	v_add_f32_e32 v226, v226, v223
	s_waitcnt vmcnt(9)
	v_and_b32_e32 v223, 0xffff0000, v216
	v_and_b32_e32 v250, 0xffff0000, v217
	v_lshlrev_b32_e32 v216, 16, v216
	v_lshlrev_b32_e32 v217, 16, v217
	v_fmac_f32_e32 v56, v244, v216
	v_fmac_f32_e32 v57, v245, v223
	v_fmac_f32_e32 v58, v246, v217
	v_fmac_f32_e32 v59, v247, v250
	v_mul_f32_e32 v223, v57, v57
	v_fmac_f32_e32 v223, v56, v56
	v_fmac_f32_e32 v223, v58, v58
	v_fmac_f32_e32 v223, v59, v59
	v_add_f32_e32 v226, v226, v223
	s_waitcnt vmcnt(2)
	v_and_b32_e32 v223, 0xffff0000, v218
	v_and_b32_e32 v250, 0xffff0000, v219
	v_lshlrev_b32_e32 v218, 16, v218
	v_lshlrev_b32_e32 v219, 16, v219
	v_fmac_f32_e32 v60, v228, v218
	v_fmac_f32_e32 v61, v229, v223
	v_fmac_f32_e32 v62, v230, v219
	v_fmac_f32_e32 v63, v231, v250
	v_mul_f32_e32 v223, v61, v61
	v_fmac_f32_e32 v223, v60, v60
	v_fmac_f32_e32 v223, v62, v62
	v_fmac_f32_e32 v223, v63, v63
	v_add_f32_e32 v226, v226, v223
	s_waitcnt vmcnt(1)
	v_and_b32_e32 v223, 0xffff0000, v220
	v_and_b32_e32 v250, 0xffff0000, v221
	v_lshlrev_b32_e32 v220, 16, v220
	v_lshlrev_b32_e32 v221, 16, v221
	v_fmac_f32_e32 v64, v232, v220
	v_fmac_f32_e32 v65, v233, v223
	v_fmac_f32_e32 v66, v234, v221
	v_fmac_f32_e32 v67, v235, v250
	v_mul_f32_e32 v223, v65, v65
	v_fmac_f32_e32 v223, v64, v64
	v_fmac_f32_e32 v223, v66, v66
	v_fmac_f32_e32 v223, v67, v67
	v_add_f32_e32 v226, v226, v223
	s_waitcnt vmcnt(0)
; #define LAS __attribute__((address_space(3)))
; DI unsigned pk_bf16(float lo, float hi) { f32x2 v = {lo, hi}; hbf16x2 r = __builtin_convertvector(v, hbf16x2); return __builtin_bit_cast(unsigned, r); }
; DI void phase_router(const Params& p, LAS unsigned char* lds, int G, int bid, const int layer, const float* xin_ctx, const float* xin_lat, const int row_lo, const int row_hi) {
;     ...
;             }
;             ss = wave_sum(ss);
;             const float r = rsqrtf(ss * (1.0f / DM) + EPS);
; #pragma unroll
;             for (int i = 0; i < 8; ++i) {
;                 const int col = 4 * lane + 256 * i;
;                 const f32x4 g = *(const f32x4*)(gain + col), sh = *(const f32x4*)(md + 3 * DM + col), scl = *(const f32x4*)(md + 4 * DM + col);
;                 const f32x4 hv = (v[i] * r * g) * (1.0f + scl) + sh;
;                 if (layer == 0 && !FP8_L0) { u32x2 w; w.x = pk_bf16(hv[0], hv[1]); w.y = pk_bf16(hv[2], hv[3]); *(u32x2*)(H + (size_t)row * DM + col) = w; }
;                 else *(unsigned*)(p.ws + WS_H8 + (size_t)row * DM + col) = pk_fp8x4(hv[0], hv[1], hv[2], hv[3]);
;                 *(LAS f32x4*)(hs + lr * RT_HS + col) = hv;
;             }
	v_and_b32_e32 v223, 0xffff0000, v224
	v_and_b32_e32 v250, 0xffff0000, v225
	v_lshlrev_b32_e32 v224, 16, v224
	v_lshlrev_b32_e32 v225, 16, v225
	v_fmac_f32_e32 v68, v236, v224
	v_fmac_f32_e32 v69, v237, v223
	v_fmac_f32_e32 v70, v238, v225
	v_fmac_f32_e32 v71, v239, v250
	v_mul_f32_e32 v223, v69, v69
	v_fmac_f32_e32 v223, v68, v68
	v_fmac_f32_e32 v223, v70, v70
	v_fmac_f32_e32 v223, v71, v71
	v_add_f32_e32 v226, v226, v223
	global_load_dwordx4 v[228:231], v27, s[100:101] offset:0
	global_load_dwordx4 v[232:235], v27, s[82:83] offset:0
	global_load_dwordx4 v[236:239], v27, s[98:99] offset:0
	global_load_dwordx4 v[240:243], v27, s[100:101] offset:1024
	global_load_dwordx4 v[244:247], v27, s[82:83] offset:1024
	global_load_dwordx4 v[216:219], v27, s[98:99] offset:1024
	global_load_dwordx4 v[2:5], v27, s[100:101] offset:2048
	global_load_dwordx4 v[6:9], v27, s[82:83] offset:2048
	global_load_dwordx2 v[248:249], v27, s[98:99] offset:2048
	global_load_dwordx2 v[220:221], v27, s[98:99] offset:2056
	ds_bpermute_b32 v223, v203, v226
	s_waitcnt lgkmcnt(0)
	v_add_f32_e32 v226, v226, v223
	ds_bpermute_b32 v223, v204, v226
	s_waitcnt lgkmcnt(0)
	v_add_f32_e32 v226, v226, v223
	ds_bpermute_b32 v223, v205, v226
	s_waitcnt lgkmcnt(0)
	v_add_f32_e32 v226, v226, v223
	ds_bpermute_b32 v223, v206, v226
	s_waitcnt lgkmcnt(0)
	v_add_f32_e32 v226, v226, v223
	ds_bpermute_b32 v223, v207, v226
	s_waitcnt lgkmcnt(0)
	v_add_f32_e32 v226, v226, v223
	ds_bpermute_b32 v223, v208, v226
	s_waitcnt lgkmcnt(0)
	v_add_f32_e32 v226, v226, v223
	v_mov_b32_e32 v250, 0x358637bd
	v_fmamk_f32 v226, v226, 0x3a000000, v250
	v_cmp_gt_f32_e32 vcc, 0x800000, v226
	v_mul_f32_e32 v223, 0x4b800000, v226
	s_nop 1
	v_cndmask_b32_e32 v226, v226, v223, vcc
	v_rsq_f32_e32 v226, v226
	s_nop 0
	v_mul_f32_e32 v223, 0x45800000, v226
	v_mov_b32_e32 v250, 0x43e00000
	v_cndmask_b32_e32 v226, v226, v223, vcc
	s_waitcnt vmcnt(7)
	v_pk_mul_f32 v[40:41], v[40:41], v[226:227] op_sel_hi:[1,0]
	v_pk_mul_f32 v[42:43], v[42:43], v[226:227] op_sel_hi:[1,0]
	v_pk_add_f32 v[236:237], v[236:237], 1.0 op_sel_hi:[1,0]
	v_pk_add_f32 v[238:239], v[238:239], 1.0 op_sel_hi:[1,0]
	v_pk_mul_f32 v[40:41], v[228:229], v[40:41]
	v_pk_mul_f32 v[42:43], v[230:231], v[42:43]
	v_pk_fma_f32 v[40:41], v[236:237], v[40:41], v[232:233]
	v_pk_fma_f32 v[42:43], v[238:239], v[42:43], v[234:235]
	v_med3_f32 v228, v40, s17, v250
	v_med3_f32 v229, v41, s17, v250
	v_med3_f32 v230, v42, s17, v250
	v_med3_f32 v231, v43, s17, v250
	ds_write_b128 v35, v[40:43] offset:0
	v_cvt_pk_fp8_f32 v224, v228, v229
	v_cvt_pk_fp8_f32 v224, v230, v231 op_sel:[0,0,1]
	s_nop 0
	global_store_dword v33, v224, s[76:77] offset:0
	global_load_dwordx4 v[228:231], v27, s[100:101] offset:3072
	global_load_dwordx4 v[232:235], v27, s[82:83] offset:3072
	global_load_dwordx4 v[236:239], v27, s[98:99] offset:3072
	s_waitcnt vmcnt(8)
	v_pk_mul_f32 v[44:45], v[44:45], v[226:227] op_sel_hi:[1,0]
	v_pk_mul_f32 v[46:47], v[46:47], v[226:227] op_sel_hi:[1,0]
	v_pk_add_f32 v[216:217], v[216:217], 1.0 op_sel_hi:[1,0]
	v_pk_add_f32 v[218:219], v[218:219], 1.0 op_sel_hi:[1,0]
	v_pk_mul_f32 v[44:45], v[240:241], v[44:45]
	v_pk_mul_f32 v[46:47], v[242:243], v[46:47]
	v_pk_fma_f32 v[44:45], v[216:217], v[44:45], v[244:245]
	v_pk_fma_f32 v[46:47], v[218:219], v[46:47], v[246:247]
	v_med3_f32 v240, v44, s17, v250
	v_med3_f32 v241, v45, s17, v250
	v_med3_f32 v242, v46, s17, v250
	v_med3_f32 v243, v47, s17, v250
	ds_write_b128 v35, v[44:47] offset:1024
	v_cvt_pk_fp8_f32 v225, v240, v241
	v_cvt_pk_fp8_f32 v225, v242, v243 op_sel:[0,0,1]
	s_nop 0
	global_store_dword v33, v225, s[76:77] offset:256
	global_load_dwordx4 v[240:243], v29, s[100:101] offset:0
	global_load_dwordx4 v[244:247], v29, s[82:83] offset:0
	global_load_dwordx4 v[216:219], v29, s[98:99] offset:0
	s_waitcnt vmcnt(8)
	v_pk_mul_f32 v[48:49], v[48:49], v[226:227] op_sel_hi:[1,0]
	v_pk_mul_f32 v[50:51], v[50:51], v[226:227] op_sel_hi:[1,0]
	v_pk_add_f32 v[248:249], v[248:249], 1.0 op_sel_hi:[1,0]
	v_pk_add_f32 v[220:221], v[220:221], 1.0 op_sel_hi:[1,0]
	v_pk_mul_f32 v[48:49], v[2:3], v[48:49]
	v_pk_mul_f32 v[50:51], v[4:5], v[50:51]
	v_pk_fma_f32 v[48:49], v[248:249], v[48:49], v[6:7]
	v_pk_fma_f32 v[50:51], v[220:221], v[50:51], v[8:9]
	v_med3_f32 v2, v48, s17, v250
	v_med3_f32 v3, v49, s17, v250
	v_med3_f32 v4, v50, s17, v250
	v_med3_f32 v5, v51, s17, v250
	ds_write_b128 v35, v[48:51] offset:2048
	v_cvt_pk_fp8_f32 v215, v2, v3
	v_cvt_pk_fp8_f32 v215, v4, v5 op_sel:[0,0,1]
	s_nop 0
	global_store_dword v33, v215, s[76:77] offset:512
	global_load_dwordx4 v[2:5], v29, s[100:101] offset:1024
	global_load_dwordx4 v[6:9], v29, s[82:83] offset:1024
	global_load_dwordx2 v[248:249], v29, s[98:99] offset:1024
	global_load_dwordx2 v[220:221], v29, s[98:99] offset:1032
	s_waitcnt vmcnt(9)
	v_pk_mul_f32 v[52:53], v[52:53], v[226:227] op_sel_hi:[1,0]
	v_pk_mul_f32 v[54:55], v[54:55], v[226:227] op_sel_hi:[1,0]
	v_pk_add_f32 v[236:237], v[236:237], 1.0 op_sel_hi:[1,0]
	v_pk_add_f32 v[238:239], v[238:239], 1.0 op_sel_hi:[1,0]
	v_pk_mul_f32 v[52:53], v[228:229], v[52:53]
	v_pk_mul_f32 v[54:55], v[230:231], v[54:55]
	v_pk_fma_f32 v[52:53], v[236:237], v[52:53], v[232:233]
	v_pk_fma_f32 v[54:55], v[238:239], v[54:55], v[234:235]
	v_med3_f32 v228, v52, s17, v250
	v_med3_f32 v229, v53, s17, v250
	v_med3_f32 v230, v54, s17, v250
	v_med3_f32 v231, v55, s17, v250
	ds_write_b128 v35, v[52:55] offset:3072
	v_cvt_pk_fp8_f32 v224, v228, v229
	v_cvt_pk_fp8_f32 v224, v230, v231 op_sel:[0,0,1]
	s_nop 0
	global_store_dword v33, v224, s[76:77] offset:768
	global_load_dwordx4 v[228:231], v29, s[100:101] offset:2048
	global_load_dwordx4 v[232:235], v29, s[82:83] offset:2048
	global_load_dwordx4 v[236:239], v29, s[98:99] offset:2048
	s_waitcnt vmcnt(9)
; #define LAS __attribute__((address_space(3)))
; DI unsigned pk_bf16(float lo, float hi) { f32x2 v = {lo, hi}; hbf16x2 r = __builtin_convertvector(v, hbf16x2); return __builtin_bit_cast(unsigned, r); }
; DI float bflo(unsigned w) { return __uint_as_float(w << 16); }
; DI float bfhi(unsigned w) { return __uint_as_float(w & 0xffff0000u); }
; DI void phase_router(const Params& p, LAS unsigned char* lds, int G, int bid, const int layer, const float* xin_ctx, const float* xin_lat, const int row_lo, const int row_hi) {
;     ...
;             const int lr = 2 * wave + rr, row = row_lo + bt * 16 + lr;
;             const float* xr = row < NCTX ? xin_ctx + (size_t)row * DM : xin_lat + (size_t)(row - NCTX) * DM;
;             const bf16_t* dr = (const bf16_t*)(p.ws + WS_D) + (size_t)row * DM;
;             const float* md = MOD + (size_t)row_mod(row) * MODN;
;             f32x4 v[8]; float ss = 0.f;
; #pragma unroll
;             for (int i = 0; i < 8; ++i) {
;                 const int col = 4 * lane + 256 * i;
;                 const u32x2 dw = *(const u32x2*)(dr + col);
;                 v[i] = *(const f32x4*)(xr + col) + *(const f32x4*)(md + 2 * DM + col) * (f32x4){bflo(dw.x), bfhi(dw.x), bflo(dw.y), bfhi(dw.y)};
;                 ss += v[i][0] * v[i][0] + v[i][1] * v[i][1] + v[i][2] * v[i][2] + v[i][3] * v[i][3];
;     ...
; #pragma unroll
;             for (int i = 0; i < 8; ++i) {
;                 const int col = 4 * lane + 256 * i;
;                 const f32x4 g = *(const f32x4*)(gain + col), sh = *(const f32x4*)(md + 3 * DM + col), scl = *(const f32x4*)(md + 4 * DM + col);
;                 const f32x4 hv = (v[i] * r * g) * (1.0f + scl) + sh;
;                 if (layer == 0 && !FP8_L0) { u32x2 w; w.x = pk_bf16(hv[0], hv[1]); w.y = pk_bf16(hv[2], hv[3]); *(u32x2*)(H + (size_t)row * DM + col) = w; }
;                 else *(unsigned*)(p.ws + WS_H8 + (size_t)row * DM + col) = pk_fp8x4(hv[0], hv[1], hv[2], hv[3]);
;                 *(LAS f32x4*)(hs + lr * RT_HS + col) = hv;
;             }
	v_pk_mul_f32 v[56:57], v[56:57], v[226:227] op_sel_hi:[1,0]
	v_pk_mul_f32 v[58:59], v[58:59], v[226:227] op_sel_hi:[1,0]
	v_pk_add_f32 v[216:217], v[216:217], 1.0 op_sel_hi:[1,0]
	v_pk_add_f32 v[218:219], v[218:219], 1.0 op_sel_hi:[1,0]
	v_pk_mul_f32 v[56:57], v[240:241], v[56:57]
	v_pk_mul_f32 v[58:59], v[242:243], v[58:59]
	v_pk_fma_f32 v[56:57], v[216:217], v[56:57], v[244:245]
	v_pk_fma_f32 v[58:59], v[218:219], v[58:59], v[246:247]
	v_med3_f32 v240, v56, s17, v250
	v_med3_f32 v241, v57, s17, v250
	v_med3_f32 v242, v58, s17, v250
	v_med3_f32 v243, v59, s17, v250
	ds_write_b128 v35, v[56:59] offset:4096
	v_cvt_pk_fp8_f32 v225, v240, v241
	v_cvt_pk_fp8_f32 v225, v242, v243 op_sel:[0,0,1]
	s_nop 0
	global_store_dword v33, v225, s[76:77] offset:1024
	global_load_dwordx4 v[240:243], v29, s[100:101] offset:3072
	global_load_dwordx4 v[244:247], v29, s[82:83] offset:3072
	global_load_dwordx4 v[216:219], v29, s[98:99] offset:3072
	s_waitcnt vmcnt(8)
	v_pk_mul_f32 v[60:61], v[60:61], v[226:227] op_sel_hi:[1,0]
	v_pk_mul_f32 v[62:63], v[62:63], v[226:227] op_sel_hi:[1,0]
	v_pk_add_f32 v[248:249], v[248:249], 1.0 op_sel_hi:[1,0]
	v_pk_add_f32 v[220:221], v[220:221], 1.0 op_sel_hi:[1,0]
	v_pk_mul_f32 v[60:61], v[2:3], v[60:61]
	v_pk_mul_f32 v[62:63], v[4:5], v[62:63]
	v_pk_fma_f32 v[60:61], v[248:249], v[60:61], v[6:7]
	v_pk_fma_f32 v[62:63], v[220:221], v[62:63], v[8:9]
	v_med3_f32 v2, v60, s17, v250
	v_med3_f32 v3, v61, s17, v250
	v_med3_f32 v4, v62, s17, v250
	v_med3_f32 v5, v63, s17, v250
	ds_write_b128 v35, v[60:63] offset:5120
	v_cvt_pk_fp8_f32 v215, v2, v3
	v_cvt_pk_fp8_f32 v215, v4, v5 op_sel:[0,0,1]
	s_nop 0
	global_store_dword v33, v215, s[76:77] offset:1280
	s_waitcnt vmcnt(5)
	v_pk_mul_f32 v[64:65], v[64:65], v[226:227] op_sel_hi:[1,0]
	v_pk_mul_f32 v[66:67], v[66:67], v[226:227] op_sel_hi:[1,0]
	v_pk_add_f32 v[236:237], v[236:237], 1.0 op_sel_hi:[1,0]
	v_pk_add_f32 v[238:239], v[238:239], 1.0 op_sel_hi:[1,0]
	v_pk_mul_f32 v[64:65], v[228:229], v[64:65]
	v_pk_mul_f32 v[66:67], v[230:231], v[66:67]
	v_pk_fma_f32 v[64:65], v[236:237], v[64:65], v[232:233]
	v_pk_fma_f32 v[66:67], v[238:239], v[66:67], v[234:235]
	v_med3_f32 v228, v64, s17, v250
	v_med3_f32 v229, v65, s17, v250
	v_med3_f32 v230, v66, s17, v250
	v_med3_f32 v231, v67, s17, v250
	ds_write_b128 v35, v[64:67] offset:6144
	v_cvt_pk_fp8_f32 v224, v228, v229
	v_cvt_pk_fp8_f32 v224, v230, v231 op_sel:[0,0,1]
	s_nop 0
	global_store_dword v33, v224, s[76:77] offset:1536
	s_waitcnt vmcnt(2)
	v_pk_mul_f32 v[68:69], v[68:69], v[226:227] op_sel_hi:[1,0]
	v_pk_mul_f32 v[70:71], v[70:71], v[226:227] op_sel_hi:[1,0]
	v_pk_add_f32 v[216:217], v[216:217], 1.0 op_sel_hi:[1,0]
	v_pk_add_f32 v[218:219], v[218:219], 1.0 op_sel_hi:[1,0]
	v_pk_mul_f32 v[68:69], v[240:241], v[68:69]
	v_pk_mul_f32 v[70:71], v[242:243], v[70:71]
	v_pk_fma_f32 v[68:69], v[216:217], v[68:69], v[244:245]
	v_pk_fma_f32 v[70:71], v[218:219], v[70:71], v[246:247]
	v_med3_f32 v240, v68, s17, v250
	v_med3_f32 v241, v69, s17, v250
	v_med3_f32 v242, v70, s17, v250
	v_med3_f32 v243, v71, s17, v250
	ds_write_b128 v35, v[68:71] offset:7168
	v_cvt_pk_fp8_f32 v225, v240, v241
	v_cvt_pk_fp8_f32 v225, v242, v243 op_sel:[0,0,1]
	s_nop 0
	global_store_dword v33, v225, s[76:77] offset:1792
	s_lshl_b32 s53, s41, 1
	s_add_i32 s53, s53, 1
	s_add_i32 s52, s40, s53
	s_mul_i32 s53, s53, 0x2010
	v_add_u32_e32 v35, s53, v27
	s_lshl_b32 s16, s52, 13
	s_add_u32 s72, s50, s16
	s_addc_u32 s73, s51, 0
	s_add_u32 s72, s72, 0x1fa0e000
	s_addc_u32 s73, s73, 0
	s_lshl_b32 s16, s52, 12
	s_add_u32 s74, s50, s16
	s_addc_u32 s75, s51, 0
	s_add_u32 s74, s74, 0x3af76000
	s_addc_u32 s75, s75, 0
	s_lshl_b32 s16, s52, 11
	s_add_u32 s76, s50, s16
	s_addc_u32 s77, s51, 0
	s_add_u32 s76, s76, 0x41b76000
	s_addc_u32 s77, s77, 0
	s_sub_i32 s16, s52, 0x400
	s_lshr_b32 s16, s16, 11
	s_cmp_lt_u32 s52, 0x400
	s_cselect_b32 s16, 4, s16
	s_mul_i32 s16, s16, 0xc000
	s_add_u32 s78, s50, s16
	s_addc_u32 s79, s51, 0
	s_add_u32 s78, s78, 0x50000
	s_addc_u32 s79, s79, 0
	s_add_u32 s82, s78, 0x2000
	s_addc_u32 s83, s79, 0
	s_add_u32 s98, s78, 0x4000
	s_addc_u32 s99, s79, 0
	global_load_dwordx2 v[2:3], v31, s[74:75] offset:0 nt
	global_load_dwordx4 v[40:43], v27, s[72:73] offset:0 nt
	global_load_dwordx4 v[228:231], v27, s[78:79] offset:0
	global_load_dwordx2 v[4:5], v31, s[74:75] offset:512 nt
	global_load_dwordx4 v[44:47], v27, s[72:73] offset:1024 nt
	global_load_dwordx4 v[232:235], v27, s[78:79] offset:1024
	global_load_dwordx2 v[6:7], v31, s[74:75] offset:1024 nt
	global_load_dwordx4 v[48:51], v27, s[72:73] offset:2048 nt
	global_load_dwordx4 v[236:239], v27, s[78:79] offset:2048
	global_load_dwordx2 v[8:9], v31, s[74:75] offset:1536 nt
	global_load_dwordx4 v[52:55], v27, s[72:73] offset:3072 nt
	global_load_dwordx4 v[240:243], v27, s[78:79] offset:3072
	global_load_dwordx2 v[216:217], v31, s[74:75] offset:2048 nt
	global_load_dwordx4 v[56:59], v29, s[72:73] offset:0 nt
	global_load_dwordx4 v[244:247], v29, s[78:79] offset:0
	global_load_dwordx2 v[218:219], v31, s[74:75] offset:2560 nt
	global_load_dwordx4 v[60:63], v29, s[72:73] offset:1024 nt
	global_load_dwordx2 v[220:221], v31, s[74:75] offset:3072 nt
	global_load_dwordx4 v[64:67], v29, s[72:73] offset:2048 nt
	global_load_dwordx2 v[224:225], v31, s[74:75] offset:3584 nt
	global_load_dwordx4 v[68:71], v29, s[72:73] offset:3072 nt
	s_waitcnt vmcnt(18)
	v_and_b32_e32 v223, 0xffff0000, v2
	v_and_b32_e32 v250, 0xffff0000, v3
	v_lshlrev_b32_e32 v2, 16, v2
	v_lshlrev_b32_e32 v3, 16, v3
	v_fmac_f32_e32 v40, v228, v2
	v_fmac_f32_e32 v41, v229, v223
	v_fmac_f32_e32 v42, v230, v3
	v_fmac_f32_e32 v43, v231, v250
	global_load_dwordx4 v[228:231], v29, s[78:79] offset:1024
	v_mul_f32_e32 v226, v41, v41
	v_fmac_f32_e32 v226, v40, v40
	v_fmac_f32_e32 v226, v42, v42
	v_fmac_f32_e32 v226, v43, v43
	s_waitcnt vmcnt(16)
; #define LAS __attribute__((address_space(3)))
; DI unsigned pk_bf16(float lo, float hi) { f32x2 v = {lo, hi}; hbf16x2 r = __builtin_convertvector(v, hbf16x2); return __builtin_bit_cast(unsigned, r); }
; DI float bflo(unsigned w) { return __uint_as_float(w << 16); }
; DI float bfhi(unsigned w) { return __uint_as_float(w & 0xffff0000u); }
; DI void phase_router(const Params& p, LAS unsigned char* lds, int G, int bid, const int layer, const float* xin_ctx, const float* xin_lat, const int row_lo, const int row_hi) {
;     ...
;             const int lr = 2 * wave + rr, row = row_lo + bt * 16 + lr;
;             const float* xr = row < NCTX ? xin_ctx + (size_t)row * DM : xin_lat + (size_t)(row - NCTX) * DM;
;             const bf16_t* dr = (const bf16_t*)(p.ws + WS_D) + (size_t)row * DM;
;             const float* md = MOD + (size_t)row_mod(row) * MODN;
;             f32x4 v[8]; float ss = 0.f;
; #pragma unroll
;             for (int i = 0; i < 8; ++i) {
;                 const int col = 4 * lane + 256 * i;
;                 const u32x2 dw = *(const u32x2*)(dr + col);
;                 v[i] = *(const f32x4*)(xr + col) + *(const f32x4*)(md + 2 * DM + col) * (f32x4){bflo(dw.x), bfhi(dw.x), bflo(dw.y), bfhi(dw.y)};
;                 ss += v[i][0] * v[i][0] + v[i][1] * v[i][1] + v[i][2] * v[i][2] + v[i][3] * v[i][3];
;             }
;             ss = wave_sum(ss);
;             const float r = rsqrtf(ss * (1.0f / DM) + EPS);
; #pragma unroll
;             for (int i = 0; i < 8; ++i) {
;                 const int col = 4 * lane + 256 * i;
;                 const f32x4 g = *(const f32x4*)(gain + col), sh = *(const f32x4*)(md + 3 * DM + col), scl = *(const f32x4*)(md + 4 * DM + col);
;                 const f32x4 hv = (v[i] * r * g) * (1.0f + scl) + sh;
;                 if (layer == 0 && !FP8_L0) { u32x2 w; w.x = pk_bf16(hv[0], hv[1]); w.y = pk_bf16(hv[2], hv[3]); *(u32x2*)(H + (size_t)row * DM + col) = w; }
;                 else *(unsigned*)(p.ws + WS_H8 + (size_t)row * DM + col) = pk_fp8x4(hv[0], hv[1], hv[2], hv[3]);
;                 *(LAS f32x4*)(hs + lr * RT_HS + col) = hv;
	v_and_b32_e32 v223, 0xffff0000, v4
	v_and_b32_e32 v250, 0xffff0000, v5
	v_lshlrev_b32_e32 v4, 16, v4
	v_lshlrev_b32_e32 v5, 16, v5
	v_fmac_f32_e32 v44, v232, v4
	v_fmac_f32_e32 v45, v233, v223
	v_fmac_f32_e32 v46, v234, v5
	v_fmac_f32_e32 v47, v235, v250
	global_load_dwordx4 v[232:235], v29, s[78:79] offset:2048
	v_mul_f32_e32 v223, v45, v45
	v_fmac_f32_e32 v223, v44, v44
	v_fmac_f32_e32 v223, v46, v46
	v_fmac_f32_e32 v223, v47, v47
	v_add_f32_e32 v226, v226, v223
	s_waitcnt vmcnt(14)
	v_and_b32_e32 v223, 0xffff0000, v6
	v_and_b32_e32 v250, 0xffff0000, v7
	v_lshlrev_b32_e32 v6, 16, v6
	v_lshlrev_b32_e32 v7, 16, v7
	v_fmac_f32_e32 v48, v236, v6
	v_fmac_f32_e32 v49, v237, v223
	v_fmac_f32_e32 v50, v238, v7
	v_fmac_f32_e32 v51, v239, v250
	global_load_dwordx4 v[236:239], v29, s[78:79] offset:3072
	v_mul_f32_e32 v223, v49, v49
	v_fmac_f32_e32 v223, v48, v48
	v_fmac_f32_e32 v223, v50, v50
	v_fmac_f32_e32 v223, v51, v51
	v_add_f32_e32 v226, v226, v223
	s_waitcnt vmcnt(12)
	v_and_b32_e32 v223, 0xffff0000, v8
	v_and_b32_e32 v250, 0xffff0000, v9
	v_lshlrev_b32_e32 v8, 16, v8
	v_lshlrev_b32_e32 v9, 16, v9
	v_fmac_f32_e32 v52, v240, v8
	v_fmac_f32_e32 v53, v241, v223
	v_fmac_f32_e32 v54, v242, v9
	v_fmac_f32_e32 v55, v243, v250
	v_mul_f32_e32 v223, v53, v53
	v_fmac_f32_e32 v223, v52, v52
	v_fmac_f32_e32 v223, v54, v54
	v_fmac_f32_e32 v223, v55, v55
	v_add_f32_e32 v226, v226, v223
	s_waitcnt vmcnt(9)
	v_and_b32_e32 v223, 0xffff0000, v216
	v_and_b32_e32 v250, 0xffff0000, v217
	v_lshlrev_b32_e32 v216, 16, v216
	v_lshlrev_b32_e32 v217, 16, v217
	v_fmac_f32_e32 v56, v244, v216
	v_fmac_f32_e32 v57, v245, v223
	v_fmac_f32_e32 v58, v246, v217
	v_fmac_f32_e32 v59, v247, v250
	v_mul_f32_e32 v223, v57, v57
	v_fmac_f32_e32 v223, v56, v56
	v_fmac_f32_e32 v223, v58, v58
	v_fmac_f32_e32 v223, v59, v59
	v_add_f32_e32 v226, v226, v223
	s_waitcnt vmcnt(2)
	v_and_b32_e32 v223, 0xffff0000, v218
	v_and_b32_e32 v250, 0xffff0000, v219
	v_lshlrev_b32_e32 v218, 16, v218
	v_lshlrev_b32_e32 v219, 16, v219
	v_fmac_f32_e32 v60, v228, v218
	v_fmac_f32_e32 v61, v229, v223
	v_fmac_f32_e32 v62, v230, v219
	v_fmac_f32_e32 v63, v231, v250
	v_mul_f32_e32 v223, v61, v61
	v_fmac_f32_e32 v223, v60, v60
	v_fmac_f32_e32 v223, v62, v62
	v_fmac_f32_e32 v223, v63, v63
	v_add_f32_e32 v226, v226, v223
	s_waitcnt vmcnt(1)
	v_and_b32_e32 v223, 0xffff0000, v220
	v_and_b32_e32 v250, 0xffff0000, v221
	v_lshlrev_b32_e32 v220, 16, v220
	v_lshlrev_b32_e32 v221, 16, v221
	v_fmac_f32_e32 v64, v232, v220
	v_fmac_f32_e32 v65, v233, v223
	v_fmac_f32_e32 v66, v234, v221
	v_fmac_f32_e32 v67, v235, v250
	v_mul_f32_e32 v223, v65, v65
	v_fmac_f32_e32 v223, v64, v64
	v_fmac_f32_e32 v223, v66, v66
	v_fmac_f32_e32 v223, v67, v67
	v_add_f32_e32 v226, v226, v223
	s_waitcnt vmcnt(0)
	v_and_b32_e32 v223, 0xffff0000, v224
	v_and_b32_e32 v250, 0xffff0000, v225
	v_lshlrev_b32_e32 v224, 16, v224
	v_lshlrev_b32_e32 v225, 16, v225
	v_fmac_f32_e32 v68, v236, v224
	v_fmac_f32_e32 v69, v237, v223
	v_fmac_f32_e32 v70, v238, v225
	v_fmac_f32_e32 v71, v239, v250
	v_mul_f32_e32 v223, v69, v69
	v_fmac_f32_e32 v223, v68, v68
	v_fmac_f32_e32 v223, v70, v70
	v_fmac_f32_e32 v223, v71, v71
	v_add_f32_e32 v226, v226, v223
	global_load_dwordx4 v[228:231], v27, s[100:101] offset:0
	global_load_dwordx4 v[232:235], v27, s[82:83] offset:0
	global_load_dwordx4 v[236:239], v27, s[98:99] offset:0
	global_load_dwordx4 v[240:243], v27, s[100:101] offset:1024
	global_load_dwordx4 v[244:247], v27, s[82:83] offset:1024
	global_load_dwordx4 v[216:219], v27, s[98:99] offset:1024
	global_load_dwordx4 v[2:5], v27, s[100:101] offset:2048
	global_load_dwordx4 v[6:9], v27, s[82:83] offset:2048
	global_load_dwordx2 v[248:249], v27, s[98:99] offset:2048
	global_load_dwordx2 v[220:221], v27, s[98:99] offset:2056
	ds_bpermute_b32 v223, v203, v226
	s_waitcnt lgkmcnt(0)
	v_add_f32_e32 v226, v226, v223
	ds_bpermute_b32 v223, v204, v226
	s_waitcnt lgkmcnt(0)
	v_add_f32_e32 v226, v226, v223
	ds_bpermute_b32 v223, v205, v226
	s_waitcnt lgkmcnt(0)
	v_add_f32_e32 v226, v226, v223
	ds_bpermute_b32 v223, v206, v226
	s_waitcnt lgkmcnt(0)
	v_add_f32_e32 v226, v226, v223
	ds_bpermute_b32 v223, v207, v226
	s_waitcnt lgkmcnt(0)
	v_add_f32_e32 v226, v226, v223
	ds_bpermute_b32 v223, v208, v226
	s_waitcnt lgkmcnt(0)
	v_add_f32_e32 v226, v226, v223
	v_mov_b32_e32 v250, 0x358637bd
	v_fmamk_f32 v226, v226, 0x3a000000, v250
	v_cmp_gt_f32_e32 vcc, 0x800000, v226
	v_mul_f32_e32 v223, 0x4b800000, v226
	s_nop 1
	v_cndmask_b32_e32 v226, v226, v223, vcc
	v_rsq_f32_e32 v226, v226
	s_nop 0
	v_mul_f32_e32 v223, 0x45800000, v226
	v_mov_b32_e32 v250, 0x43e00000
	v_cndmask_b32_e32 v226, v226, v223, vcc
	s_waitcnt vmcnt(7)
	v_pk_mul_f32 v[40:41], v[40:41], v[226:227] op_sel_hi:[1,0]
	v_pk_mul_f32 v[42:43], v[42:43], v[226:227] op_sel_hi:[1,0]
	v_pk_add_f32 v[236:237], v[236:237], 1.0 op_sel_hi:[1,0]
	v_pk_add_f32 v[238:239], v[238:239], 1.0 op_sel_hi:[1,0]
	v_pk_mul_f32 v[40:41], v[228:229], v[40:41]
	v_pk_mul_f32 v[42:43], v[230:231], v[42:43]
	v_pk_fma_f32 v[40:41], v[236:237], v[40:41], v[232:233]
	v_pk_fma_f32 v[42:43], v[238:239], v[42:43], v[234:235]
	v_med3_f32 v228, v40, s17, v250
	v_med3_f32 v229, v41, s17, v250
	v_med3_f32 v230, v42, s17, v250
	v_med3_f32 v231, v43, s17, v250
	ds_write_b128 v35, v[40:43] offset:0
	v_cvt_pk_fp8_f32 v224, v228, v229
	v_cvt_pk_fp8_f32 v224, v230, v231 op_sel:[0,0,1]
	s_nop 0
	global_store_dword v33, v224, s[76:77] offset:0
	global_load_dwordx4 v[228:231], v27, s[100:101] offset:3072
	global_load_dwordx4 v[232:235], v27, s[82:83] offset:3072
	global_load_dwordx4 v[236:239], v27, s[98:99] offset:3072
	s_waitcnt vmcnt(8)
; #define LAS __attribute__((address_space(3)))
; DI unsigned pk_bf16(float lo, float hi) { f32x2 v = {lo, hi}; hbf16x2 r = __builtin_convertvector(v, hbf16x2); return __builtin_bit_cast(unsigned, r); }
; DI void phase_router(const Params& p, LAS unsigned char* lds, int G, int bid, const int layer, const float* xin_ctx, const float* xin_lat, const int row_lo, const int row_hi) {
;     ...
; #pragma unroll
;             for (int i = 0; i < 8; ++i) {
;                 const int col = 4 * lane + 256 * i;
;                 const f32x4 g = *(const f32x4*)(gain + col), sh = *(const f32x4*)(md + 3 * DM + col), scl = *(const f32x4*)(md + 4 * DM + col);
;                 const f32x4 hv = (v[i] * r * g) * (1.0f + scl) + sh;
;                 if (layer == 0 && !FP8_L0) { u32x2 w; w.x = pk_bf16(hv[0], hv[1]); w.y = pk_bf16(hv[2], hv[3]); *(u32x2*)(H + (size_t)row * DM + col) = w; }
;                 else *(unsigned*)(p.ws + WS_H8 + (size_t)row * DM + col) = pk_fp8x4(hv[0], hv[1], hv[2], hv[3]);
;                 *(LAS f32x4*)(hs + lr * RT_HS + col) = hv;
	v_pk_mul_f32 v[44:45], v[44:45], v[226:227] op_sel_hi:[1,0]
	v_pk_mul_f32 v[46:47], v[46:47], v[226:227] op_sel_hi:[1,0]
	v_pk_add_f32 v[216:217], v[216:217], 1.0 op_sel_hi:[1,0]
	v_pk_add_f32 v[218:219], v[218:219], 1.0 op_sel_hi:[1,0]
	v_pk_mul_f32 v[44:45], v[240:241], v[44:45]
	v_pk_mul_f32 v[46:47], v[242:243], v[46:47]
	v_pk_fma_f32 v[44:45], v[216:217], v[44:45], v[244:245]
	v_pk_fma_f32 v[46:47], v[218:219], v[46:47], v[246:247]
	v_med3_f32 v240, v44, s17, v250
	v_med3_f32 v241, v45, s17, v250
	v_med3_f32 v242, v46, s17, v250
	v_med3_f32 v243, v47, s17, v250
	ds_write_b128 v35, v[44:47] offset:1024
	v_cvt_pk_fp8_f32 v225, v240, v241
	v_cvt_pk_fp8_f32 v225, v242, v243 op_sel:[0,0,1]
	s_nop 0
	global_store_dword v33, v225, s[76:77] offset:256
	global_load_dwordx4 v[240:243], v29, s[100:101] offset:0
	global_load_dwordx4 v[244:247], v29, s[82:83] offset:0
	global_load_dwordx4 v[216:219], v29, s[98:99] offset:0
	s_waitcnt vmcnt(8)
	v_pk_mul_f32 v[48:49], v[48:49], v[226:227] op_sel_hi:[1,0]
	v_pk_mul_f32 v[50:51], v[50:51], v[226:227] op_sel_hi:[1,0]
	v_pk_add_f32 v[248:249], v[248:249], 1.0 op_sel_hi:[1,0]
	v_pk_add_f32 v[220:221], v[220:221], 1.0 op_sel_hi:[1,0]
	v_pk_mul_f32 v[48:49], v[2:3], v[48:49]
	v_pk_mul_f32 v[50:51], v[4:5], v[50:51]
	v_pk_fma_f32 v[48:49], v[248:249], v[48:49], v[6:7]
	v_pk_fma_f32 v[50:51], v[220:221], v[50:51], v[8:9]
	v_med3_f32 v2, v48, s17, v250
	v_med3_f32 v3, v49, s17, v250
	v_med3_f32 v4, v50, s17, v250
	v_med3_f32 v5, v51, s17, v250
	ds_write_b128 v35, v[48:51] offset:2048
	v_cvt_pk_fp8_f32 v215, v2, v3
	v_cvt_pk_fp8_f32 v215, v4, v5 op_sel:[0,0,1]
	s_nop 0
	global_store_dword v33, v215, s[76:77] offset:512
	global_load_dwordx4 v[2:5], v29, s[100:101] offset:1024
	global_load_dwordx4 v[6:9], v29, s[82:83] offset:1024
	global_load_dwordx2 v[248:249], v29, s[98:99] offset:1024
	global_load_dwordx2 v[220:221], v29, s[98:99] offset:1032
	s_waitcnt vmcnt(9)
	v_pk_mul_f32 v[52:53], v[52:53], v[226:227] op_sel_hi:[1,0]
	v_pk_mul_f32 v[54:55], v[54:55], v[226:227] op_sel_hi:[1,0]
	v_pk_add_f32 v[236:237], v[236:237], 1.0 op_sel_hi:[1,0]
	v_pk_add_f32 v[238:239], v[238:239], 1.0 op_sel_hi:[1,0]
	v_pk_mul_f32 v[52:53], v[228:229], v[52:53]
	v_pk_mul_f32 v[54:55], v[230:231], v[54:55]
	v_pk_fma_f32 v[52:53], v[236:237], v[52:53], v[232:233]
	v_pk_fma_f32 v[54:55], v[238:239], v[54:55], v[234:235]
	v_med3_f32 v228, v52, s17, v250
	v_med3_f32 v229, v53, s17, v250
	v_med3_f32 v230, v54, s17, v250
	v_med3_f32 v231, v55, s17, v250
	ds_write_b128 v35, v[52:55] offset:3072
	v_cvt_pk_fp8_f32 v224, v228, v229
	v_cvt_pk_fp8_f32 v224, v230, v231 op_sel:[0,0,1]
	s_nop 0
	global_store_dword v33, v224, s[76:77] offset:768
	global_load_dwordx4 v[228:231], v29, s[100:101] offset:2048
	global_load_dwordx4 v[232:235], v29, s[82:83] offset:2048
	global_load_dwordx4 v[236:239], v29, s[98:99] offset:2048
	s_waitcnt vmcnt(9)
	v_pk_mul_f32 v[56:57], v[56:57], v[226:227] op_sel_hi:[1,0]
	v_pk_mul_f32 v[58:59], v[58:59], v[226:227] op_sel_hi:[1,0]
	v_pk_add_f32 v[216:217], v[216:217], 1.0 op_sel_hi:[1,0]
	v_pk_add_f32 v[218:219], v[218:219], 1.0 op_sel_hi:[1,0]
	v_pk_mul_f32 v[56:57], v[240:241], v[56:57]
	v_pk_mul_f32 v[58:59], v[242:243], v[58:59]
	v_pk_fma_f32 v[56:57], v[216:217], v[56:57], v[244:245]
	v_pk_fma_f32 v[58:59], v[218:219], v[58:59], v[246:247]
	v_med3_f32 v240, v56, s17, v250
	v_med3_f32 v241, v57, s17, v250
	v_med3_f32 v242, v58, s17, v250
	v_med3_f32 v243, v59, s17, v250
	ds_write_b128 v35, v[56:59] offset:4096
	v_cvt_pk_fp8_f32 v225, v240, v241
	v_cvt_pk_fp8_f32 v225, v242, v243 op_sel:[0,0,1]
	s_nop 0
	global_store_dword v33, v225, s[76:77] offset:1024
	global_load_dwordx4 v[240:243], v29, s[100:101] offset:3072
	global_load_dwordx4 v[244:247], v29, s[82:83] offset:3072
	global_load_dwordx4 v[216:219], v29, s[98:99] offset:3072
	s_waitcnt vmcnt(8)
	v_pk_mul_f32 v[60:61], v[60:61], v[226:227] op_sel_hi:[1,0]
	v_pk_mul_f32 v[62:63], v[62:63], v[226:227] op_sel_hi:[1,0]
	v_pk_add_f32 v[248:249], v[248:249], 1.0 op_sel_hi:[1,0]
	v_pk_add_f32 v[220:221], v[220:221], 1.0 op_sel_hi:[1,0]
	v_pk_mul_f32 v[60:61], v[2:3], v[60:61]
	v_pk_mul_f32 v[62:63], v[4:5], v[62:63]
	v_pk_fma_f32 v[60:61], v[248:249], v[60:61], v[6:7]
	v_pk_fma_f32 v[62:63], v[220:221], v[62:63], v[8:9]
	v_med3_f32 v2, v60, s17, v250
	v_med3_f32 v3, v61, s17, v250
	v_med3_f32 v4, v62, s17, v250
	v_med3_f32 v5, v63, s17, v250
	ds_write_b128 v35, v[60:63] offset:5120
	v_cvt_pk_fp8_f32 v215, v2, v3
	v_cvt_pk_fp8_f32 v215, v4, v5 op_sel:[0,0,1]
	s_nop 0
	global_store_dword v33, v215, s[76:77] offset:1280
	s_waitcnt vmcnt(5)
	v_pk_mul_f32 v[64:65], v[64:65], v[226:227] op_sel_hi:[1,0]
	v_pk_mul_f32 v[66:67], v[66:67], v[226:227] op_sel_hi:[1,0]
	v_pk_add_f32 v[236:237], v[236:237], 1.0 op_sel_hi:[1,0]
	v_pk_add_f32 v[238:239], v[238:239], 1.0 op_sel_hi:[1,0]
	v_pk_mul_f32 v[64:65], v[228:229], v[64:65]
	v_pk_mul_f32 v[66:67], v[230:231], v[66:67]
	v_pk_fma_f32 v[64:65], v[236:237], v[64:65], v[232:233]
	v_pk_fma_f32 v[66:67], v[238:239], v[66:67], v[234:235]
	v_med3_f32 v228, v64, s17, v250
	v_med3_f32 v229, v65, s17, v250
	v_med3_f32 v230, v66, s17, v250
	v_med3_f32 v231, v67, s17, v250
	ds_write_b128 v35, v[64:67] offset:6144
	v_cvt_pk_fp8_f32 v224, v228, v229
	v_cvt_pk_fp8_f32 v224, v230, v231 op_sel:[0,0,1]
	s_nop 0
	global_store_dword v33, v224, s[76:77] offset:1536
	s_waitcnt vmcnt(2)
	v_pk_mul_f32 v[68:69], v[68:69], v[226:227] op_sel_hi:[1,0]
	v_pk_mul_f32 v[70:71], v[70:71], v[226:227] op_sel_hi:[1,0]
	v_pk_add_f32 v[216:217], v[216:217], 1.0 op_sel_hi:[1,0]
	v_pk_add_f32 v[218:219], v[218:219], 1.0 op_sel_hi:[1,0]
	v_pk_mul_f32 v[68:69], v[240:241], v[68:69]
	v_pk_mul_f32 v[70:71], v[242:243], v[70:71]
	v_pk_fma_f32 v[68:69], v[216:217], v[68:69], v[244:245]
	v_pk_fma_f32 v[70:71], v[218:219], v[70:71], v[246:247]
	v_med3_f32 v240, v68, s17, v250
	v_med3_f32 v241, v69, s17, v250
	v_med3_f32 v242, v70, s17, v250
	v_med3_f32 v243, v71, s17, v250
	ds_write_b128 v35, v[68:71] offset:7168
	v_cvt_pk_fp8_f32 v225, v240, v241
	v_cvt_pk_fp8_f32 v225, v242, v243 op_sel:[0,0,1]
	s_nop 0
	global_store_dword v33, v225, s[76:77] offset:1792
	s_branch .LBB0_1512

; __global__ void __launch_bounds__(NTHREADS, 2) fwd_kernel(Params p) {
	.amdhsa_kernel _Z10fwd_kernel6Params
		.amdhsa_group_segment_fixed_size 0
		.amdhsa_private_segment_fixed_size 0
		.amdhsa_kernarg_size 592
		.amdhsa_user_sgpr_count 2
		.amdhsa_user_sgpr_dispatch_ptr 0
		.amdhsa_user_sgpr_queue_ptr 0
		.amdhsa_user_sgpr_kernarg_segment_ptr 1
		.amdhsa_user_sgpr_dispatch_id 0
		.amdhsa_user_sgpr_kernarg_preload_length 0
		.amdhsa_user_sgpr_kernarg_preload_offset 0
		.amdhsa_user_sgpr_private_segment_size 0
		.amdhsa_uses_dynamic_stack 0
		.amdhsa_enable_private_segment 0
		.amdhsa_system_sgpr_workgroup_id_x 1
		.amdhsa_system_sgpr_workgroup_id_y 0
		.amdhsa_system_sgpr_workgroup_id_z 0
		.amdhsa_system_sgpr_workgroup_info 0
		.amdhsa_system_vgpr_workitem_id 0
		.amdhsa_next_free_vgpr 252
		.amdhsa_next_free_sgpr 102
		.amdhsa_accum_offset 252
		.amdhsa_reserve_vcc 1
		.amdhsa_float_round_mode_32 0
		.amdhsa_float_round_mode_16_64 0
		.amdhsa_float_denorm_mode_32 3
		.amdhsa_float_denorm_mode_16_64 3
		.amdhsa_dx10_clamp 1
		.amdhsa_ieee_mode 1
		.amdhsa_fp16_overflow 0
		.amdhsa_tg_split 0
		.amdhsa_exception_fp_ieee_invalid_op 0
		.amdhsa_exception_fp_denorm_src 0
		.amdhsa_exception_fp_ieee_div_zero 0
		.amdhsa_exception_fp_ieee_overflow 0
		.amdhsa_exception_fp_ieee_underflow 0
		.amdhsa_exception_fp_ieee_inexact 0
		.amdhsa_exception_int_div_zero 0
	.end_amdhsa_kernel

; __global__ void __launch_bounds__(NTHREADS, 2) fwd_kernel(Params p) {
amdhsa.kernels:
  - .agpr_count:     0
    .args:
      - .offset:         0
        .size:           336
        .value_kind:     by_value
      - .offset:         336
        .size:           4
        .value_kind:     hidden_block_count_x
      - .offset:         340
        .size:           4
        .value_kind:     hidden_block_count_y
      - .offset:         344
        .size:           4
        .value_kind:     hidden_block_count_z
      - .offset:         348
        .size:           2
        .value_kind:     hidden_group_size_x
      - .offset:         350
        .size:           2
        .value_kind:     hidden_group_size_y
      - .offset:         352
        .size:           2
        .value_kind:     hidden_group_size_z
      - .offset:         354
        .size:           2
        .value_kind:     hidden_remainder_x
      - .offset:         356
        .size:           2
        .value_kind:     hidden_remainder_y
      - .offset:         358
        .size:           2
        .value_kind:     hidden_remainder_z
      - .offset:         376
        .size:           8
        .value_kind:     hidden_global_offset_x
      - .offset:         384
        .size:           8
        .value_kind:     hidden_global_offset_y
      - .offset:         392
        .size:           8
        .value_kind:     hidden_global_offset_z
      - .offset:         400
        .size:           2
        .value_kind:     hidden_grid_dims
      - .offset:         456
        .size:           4
        .value_kind:     hidden_dynamic_lds_size
    .group_segment_fixed_size: 0
    .kernarg_segment_align: 8
    .kernarg_segment_size: 592
    .language:       OpenCL C
    .language_version:
      - 2
      - 0
    .max_flat_workgroup_size: 512
    .name:           _Z10fwd_kernel6Params
    .private_segment_fixed_size: 0
    .sgpr_count:     108
    .sgpr_spill_count: 48
    .symbol:         _Z10fwd_kernel6Params.kd
    .uniform_work_group_size: 1
    .uses_dynamic_stack: false
    .vgpr_count:     252
    .vgpr_spill_count: 0
    .wavefront_size: 64
